# speedup vs baseline: 1.0065x; 1.0010x over previous
.LBB1_7:
	s_or_b64 exec, exec, s[2:3]
	v_mov_b32_e32 v10, v167
	s_waitcnt lgkmcnt(0)
	s_barrier
	s_waitcnt vmcnt(18)
	s_ashr_i32 s2, s4, 6
	s_lshl_b32 s3, s2, 3
	s_and_b32 s5, s3, 8
	s_bfe_u32 s26, s2, 0x10001
	s_or_b32 s5, s26, s5
	s_lshl_b32 s26, s2, 9
	s_and_b32 s26, s26, 0x400
	s_lshl_b32 s5, s5, 4
	s_or_b32 s28, s5, s26
	v_lshrrev_b32_e32 v182, 5, v167
	v_bfe_u32 v2, v156, 4, 1
	v_bitop3_b32 v3, v182, v156, 1 bitop3:0x78
	v_lshlrev_b32_e32 v154, 2, v182
	v_xor_b32_e32 v3, v3, v2
	v_bitop3_b32 v4, v154, v156, 4 bitop3:0x78
	v_and_b32_e32 v5, 10, v156
	v_or3_b32 v3, v5, v4, v3
	s_lshl_b32 s5, s2, 4
	v_lshlrev_b32_e32 v3, 4, v3
	s_lshl_b32 s3, s2, 13
	s_and_b32 s29, s5, 16
	v_lshlrev_b32_e32 v170, 8, v182
	v_lshl_or_b32 v171, v2, 10, v3
	s_or_b32 s26, s29, s3
	v_bitop3_b32 v179, v171, s26, v170 bitop3:0x36
	s_or_b32 s5, s26, 0x280
	v_bitop3_b32 v178, v171, s5, v170 bitop3:0x36
	s_or_b32 s30, s3, 0x800
	s_or_b32 s33, s3, 0x1000
	s_or_b32 s29, s29, 64
	s_or_b32 s34, s29, s33
	v_bitop3_b32 v180, v171, s34, v170 bitop3:0x36
	s_or_b32 s29, s3, s29
	s_or_b32 s29, s29, 0x1280
	s_and_b32 s5, s2, 1
	s_lshl_b32 s31, s5, 4
	s_or_b32 s2, s31, s3
	v_bitop3_b32 v173, v171, s2, v170 bitop3:0x36
	v_bitop3_b32 v34, v156, 31, v156 bitop3:0xc
	v_lshrrev_b32_e32 v35, 4, v34
	v_bitop3_b32 v36, v34, v182, 1 bitop3:0x6c
	v_xor_b32_e32 v36, v36, v35
	v_bitop3_b32 v34, v34, v154, 4 bitop3:0x6c
	v_bitop3_b32 v37, v156, 10, 31 bitop3:8
	v_or3_b32 v34, v37, v34, v36
	v_lshlrev_b32_e32 v35, 10, v35
	v_lshlrev_b32_e32 v34, 4, v34
	v_or3_b32 v154, v35, v34, v170
	v_bitop3_b32 v172, s2, v154, v159 bitop3:0x36
	v_bitop3_b32 v176, v171, s29, v170 bitop3:0x36
	s_or_b32 s29, s31, s30
	s_or_b32 s29, s29, 0xa0
	v_bitop3_b32 v175, v171, s29, v170 bitop3:0x36
	s_or_b32 s29, s2, 0xaa0
	s_xor_b32 s29, s29, 0x80
	v_xor_b32_e32 v174, s29, v154
	s_or_b32 s29, s26, 0x18e0
	v_bitop3_b32 v181, v171, s29, v170 bitop3:0x36
	s_or_b32 s29, s26, 0x1a60
	v_bitop3_b32 v177, v171, s29, v170 bitop3:0x36
	s_or_b32 s29, s31, 64
	s_or_b32 s3, s3, s29
	s_mov_b32 s41, s3
	s_or_b32 s29, s29, s33
	s_mov_b32 s40, s29
	s_or_b32 s3, s2, 0x18e0
	s_mov_b32 s42, s3
	s_or_b32 s2, s2, 0x1ae0
	s_xor_b32 s2, s2, 0x80
	s_mov_b32 s43, s2
	s_lshr_b32 s38, s4, 1
	v_and_b32_e32 v26, 31, v167
	v_and_b32_e32 v27, 3, v167
	v_bfe_u32 v28, v167, 3, 1
	v_bfe_u32 v29, v167, 2, 1
	v_lshl_or_b32 v27, v28, 2, v27
	v_lshl_or_b32 v27, v29, 3, v27
	v_lshlrev_b32_e32 v32, 9, v182
	v_lshl_add_u32 v30, v27, 3, v32
	v_add_u32_e32 v30, 0x10000, v30
	v_lshl_add_u32 v31, v26, 3, v32
	v_add_u32_e32 v31, 0x10400, v31
	v_xor_b32_e32 v28, 31, v26
	v_lshl_add_u32 v28, v28, 3, v32
	v_add_u32_e32 v28, 0x10400, v28
	v_bfe_u32 v29, v167, 4, 1
	v_mul_u32_u24_e32 v29, 0x78, v29
	v_xor_b32_e32 v254, s38, v29
	v_or_b32_e32 v254, 0x10800, v254
	v_and_b32_e32 v33, 16, v167
	v_cmp_eq_u32_e32 vcc, 0, v33
	ds_read2_b64 v[66:69], v30 offset0:0 offset1:32
	ds_read2_b64 v[70:73], v30 offset0:16 offset1:48
	ds_read2_b64 v[230:233], v31 offset0:0 offset1:32
	ds_read2_b64 v[234:237], v28 offset0:0 offset1:32
	ds_read2_b64 v[238:241], v254 offset0:0 offset1:16
	ds_read2_b64 v[242:245], v254 offset0:32 offset1:48
	s_waitcnt lgkmcnt(0)
	v_cndmask_b32_e32 v74, v67, v66, vcc
	v_cndmask_b32_e32 v75, v69, v68, vcc
	v_cndmask_b32_e64 v76, v66, -v67, vcc
	v_cndmask_b32_e64 v77, v68, -v69, vcc
	v_cndmask_b32_e32 v78, v71, v70, vcc
	v_cndmask_b32_e32 v79, v73, v72, vcc
	v_cndmask_b32_e64 v80, v70, -v71, vcc
	v_cndmask_b32_e64 v81, v72, -v73, vcc
	v_cvt_pk_f16_f32 v222, v74, v75
	v_cvt_pk_f16_f32 v223, v74, v75
	v_cvt_pk_f16_f32 v224, v76, v77
	v_cvt_pk_f16_f32 v225, v76, v77
	v_cvt_pk_f16_f32 v226, v78, v79
	v_cvt_pk_f16_f32 v227, v78, v79
	v_cvt_pk_f16_f32 v228, v80, v81
	v_cvt_pk_f16_f32 v229, v80, v81
	v_mul_f32_e32 v66, v231, v239
	v_mul_f32_e32 v68, v231, v238
	v_mul_f32_e32 v67, v231, v241
	v_mul_f32_e32 v69, v231, v240
	v_fma_f32 v66, v230, v238, -v66
	v_fma_f32 v68, v230, v239, v68
	v_fma_f32 v67, v230, v240, -v67
	v_fma_f32 v69, v230, v241, v69
	v_cvt_pk_f16_f32 v246, v66, v67
	v_cvt_pk_f16_f32 v248, v68, v69
	v_mul_f32_e32 v70, v233, v243
	v_mul_f32_e32 v72, v233, v242
	v_mul_f32_e32 v71, v233, v245
	v_mul_f32_e32 v73, v233, v244
	v_fma_f32 v70, v232, v242, -v70
	v_fma_f32 v72, v232, v243, v72
	v_fma_f32 v71, v232, v244, -v71
	v_fma_f32 v73, v232, v245, v73
	v_cvt_pk_f16_f32 v247, v70, v71
	v_cvt_pk_f16_f32 v249, v72, v73
	v_mul_f32_e32 v66, v235, v239
	v_mul_f32_e32 v68, v235, v238
	v_mul_f32_e32 v67, v235, v241
	v_mul_f32_e32 v69, v235, v240
	v_fma_f32 v66, v234, v238, -v66
	v_fma_f32 v68, v234, v239, v68
	v_fma_f32 v67, v234, v240, -v67
	v_fma_f32 v69, v234, v241, v69
	v_cvt_pk_f16_f32 v250, v66, v67
	v_cvt_pk_f16_f32 v252, v68, v69
	v_mul_f32_e32 v70, v237, v243
	v_mul_f32_e32 v72, v237, v242
	v_mul_f32_e32 v71, v237, v245
	v_mul_f32_e32 v73, v237, v244
	v_fma_f32 v70, v236, v242, -v70
	v_fma_f32 v72, v236, v243, v72
	v_fma_f32 v71, v236, v244, -v71
	v_fma_f32 v73, v236, v245, v73
	v_cvt_pk_f16_f32 v251, v70, v71
	v_cvt_pk_f16_f32 v253, v72, v73
	v_xor_b32_e32 v255, 8, v254
	ds_read2_b64 v[238:241], v255 offset0:0 offset1:16
	ds_read2_b64 v[242:245], v255 offset0:32 offset1:48
	v_mfma_f32_32x32x16_f16 v[2:17], v[222:225], v[246:249], 0
	v_mfma_f32_32x32x16_f16 v[18:33], v[226:229], v[250:253], 0
	s_waitcnt lgkmcnt(0)
	v_mul_f32_e32 v66, v231, v239
	v_mul_f32_e32 v68, v231, v238
	v_mul_f32_e32 v67, v231, v241
	v_mul_f32_e32 v69, v231, v240
	v_fma_f32 v66, v230, v238, -v66
	v_fma_f32 v68, v230, v239, v68
	v_fma_f32 v67, v230, v240, -v67
	v_fma_f32 v69, v230, v241, v69
	v_cvt_pk_f16_f32 v246, v66, v67
	v_cvt_pk_f16_f32 v248, v68, v69
	v_mul_f32_e32 v70, v233, v243
	v_mul_f32_e32 v72, v233, v242
	v_mul_f32_e32 v71, v233, v245
	v_mul_f32_e32 v73, v233, v244
	v_fma_f32 v70, v232, v242, -v70
	v_fma_f32 v72, v232, v243, v72
	v_fma_f32 v71, v232, v244, -v71
	v_fma_f32 v73, v232, v245, v73
	v_cvt_pk_f16_f32 v247, v70, v71
	v_cvt_pk_f16_f32 v249, v72, v73
	v_cvt_pk_f16_f32 v2, v2, v3
	v_cvt_pk_f16_f32 v3, v4, v5
	v_cvt_pk_f16_f32 v4, v6, v7
	v_cvt_pk_f16_f32 v5, v8, v9
	v_cvt_pk_f16_f32 v6, v10, v11
	v_cvt_pk_f16_f32 v7, v12, v13
	v_cvt_pk_f16_f32 v8, v14, v15
	v_cvt_pk_f16_f32 v9, v16, v17
	v_cvt_pk_f16_f32 v18, v18, v19
	v_cvt_pk_f16_f32 v19, v20, v21
	v_cvt_pk_f16_f32 v20, v22, v23
	v_cvt_pk_f16_f32 v21, v24, v25
	v_cvt_pk_f16_f32 v22, v26, v27
	v_cvt_pk_f16_f32 v23, v28, v29
	v_cvt_pk_f16_f32 v24, v30, v31
	v_cvt_pk_f16_f32 v25, v32, v33
	s_setprio 1
	s_waitcnt vmcnt(14)
	v_mul_f32_e32 v66, v235, v239
	v_mul_f32_e32 v68, v235, v238
	v_mfma_f32_32x32x16_f16 v[34:49], v[2:5], v[150:153], 0
	v_mul_f32_e32 v67, v235, v241
	v_mul_f32_e32 v69, v235, v240
	v_mfma_f32_32x32x16_f16 v[34:49], v[18:21], v[146:149], v[34:49]
	v_fma_f32 v66, v234, v238, -v66
	v_fma_f32 v68, v234, v239, v68
	v_mfma_f32_32x32x16_f16 v[34:49], v[6:9], v[142:145], v[34:49]
	v_fma_f32 v67, v234, v240, -v67
	v_fma_f32 v69, v234, v241, v69
	v_mfma_f32_32x32x16_f16 v[34:49], v[22:25], v[138:141], v[34:49]
	v_cvt_pk_f16_f32 v250, v66, v67
	v_cvt_pk_f16_f32 v252, v68, v69
	s_waitcnt vmcnt(5)
	v_mul_f32_e32 v70, v237, v243
	v_mul_f32_e32 v72, v237, v242
	v_mfma_f32_32x32x16_f16 v[50:65], v[2:5], v[134:137], 0
	v_mul_f32_e32 v71, v237, v245
	v_mul_f32_e32 v73, v237, v244
	v_mfma_f32_32x32x16_f16 v[50:65], v[18:21], v[126:129], v[50:65]
	v_fma_f32 v70, v236, v242, -v70
	v_fma_f32 v72, v236, v243, v72
	v_mfma_f32_32x32x16_f16 v[50:65], v[6:9], v[122:125], v[50:65]
	v_fma_f32 v71, v236, v244, -v71
	v_fma_f32 v73, v236, v245, v73
	v_mfma_f32_32x32x16_f16 v[50:65], v[22:25], v[130:133], v[50:65]
	v_cvt_pk_f16_f32 v251, v70, v71
	v_cvt_pk_f16_f32 v253, v72, v73
	v_xor_b32_e32 v255, 16, v254
	ds_read2_b64 v[238:241], v255 offset0:0 offset1:16
	ds_read2_b64 v[242:245], v255 offset0:32 offset1:48
	v_mfma_f32_32x32x16_f16 v[2:17], v[222:225], v[246:249], 0
	v_mfma_f32_32x32x16_f16 v[18:33], v[226:229], v[250:253], 0
	v_cvt_pk_f16_f32 v34, v34, v35
	v_cvt_pk_f16_f32 v35, v36, v37
	v_cvt_pk_f16_f32 v36, v38, v39
	v_cvt_pk_f16_f32 v37, v40, v41
	v_cvt_pk_f16_f32 v38, v42, v43
	v_cvt_pk_f16_f32 v39, v44, v45
	v_cvt_pk_f16_f32 v40, v46, v47
	v_cvt_pk_f16_f32 v41, v48, v49
	v_cvt_pk_f16_f32 v50, v50, v51
	v_cvt_pk_f16_f32 v51, v52, v53
	v_cvt_pk_f16_f32 v52, v54, v55
	v_cvt_pk_f16_f32 v53, v56, v57
	v_cvt_pk_f16_f32 v54, v58, v59
	v_cvt_pk_f16_f32 v55, v60, v61
	v_cvt_pk_f16_f32 v56, v62, v63
	v_cvt_pk_f16_f32 v57, v64, v65
	s_waitcnt vmcnt(2)
	v_cvt_pk_f16_f32 v2, v2, v3
	v_cvt_pk_f16_f32 v3, v4, v5
	v_cvt_pk_f16_f32 v4, v6, v7
	v_cvt_pk_f16_f32 v5, v8, v9
	v_mfma_f32_32x32x16_f16 v[190:205], v[34:37], v[118:121], 0
	v_cvt_pk_f16_f32 v6, v10, v11
	v_cvt_pk_f16_f32 v7, v12, v13
	v_cvt_pk_f16_f32 v8, v14, v15
	v_cvt_pk_f16_f32 v9, v16, v17
	v_mfma_f32_32x32x16_f16 v[206:221], v[34:37], v[102:105], 0
	v_cvt_pk_f16_f32 v18, v18, v19
	v_cvt_pk_f16_f32 v19, v20, v21
	v_cvt_pk_f16_f32 v20, v22, v23
	v_cvt_pk_f16_f32 v21, v24, v25
	v_mfma_f32_32x32x16_f16 v[190:205], v[38:41], v[114:117], v[190:205]
	v_cvt_pk_f16_f32 v22, v26, v27
	v_cvt_pk_f16_f32 v23, v28, v29
	v_cvt_pk_f16_f32 v24, v30, v31
	v_cvt_pk_f16_f32 v25, v32, v33
	v_mfma_f32_32x32x16_f16 v[206:221], v[38:41], v[98:101], v[206:221]
	s_waitcnt lgkmcnt(0)
	v_mul_f32_e32 v66, v231, v239
	v_mul_f32_e32 v68, v231, v238
	v_mul_f32_e32 v67, v231, v241
	v_mfma_f32_32x32x16_f16 v[190:205], v[50:53], v[110:113], v[190:205]
	v_mul_f32_e32 v69, v231, v240
	v_fma_f32 v66, v230, v238, -v66
	v_fma_f32 v68, v230, v239, v68
	v_fma_f32 v67, v230, v240, -v67
	v_mfma_f32_32x32x16_f16 v[206:221], v[50:53], v[94:97], v[206:221]
	v_fma_f32 v69, v230, v241, v69
	v_cvt_pk_f16_f32 v246, v66, v67
	v_cvt_pk_f16_f32 v248, v68, v69
	v_mul_f32_e32 v70, v233, v243
	v_mfma_f32_32x32x16_f16 v[190:205], v[54:57], v[106:109], v[190:205]
	v_mul_f32_e32 v72, v233, v242
	v_mul_f32_e32 v71, v233, v245
	v_mul_f32_e32 v73, v233, v244
	v_fma_f32 v70, v232, v242, -v70
	v_mfma_f32_32x32x16_f16 v[206:221], v[54:57], v[90:93], v[206:221]
	v_fma_f32 v72, v232, v243, v72
	v_fma_f32 v71, v232, v244, -v71
	v_fma_f32 v73, v232, v245, v73
	v_cvt_pk_f16_f32 v247, v70, v71
	v_cvt_pk_f16_f32 v249, v72, v73
	v_mfma_f32_32x32x16_f16 v[34:49], v[2:5], v[150:153], 0
	v_mul_f32_e32 v66, v235, v239
	v_mul_f32_e32 v68, v235, v238
	v_mul_f32_e32 v67, v235, v241
	v_mul_f32_e32 v69, v235, v240
	v_fma_f32 v66, v234, v238, -v66
	v_mfma_f32_32x32x16_f16 v[34:49], v[18:21], v[146:149], v[34:49]
	v_fma_f32 v68, v234, v239, v68
	v_fma_f32 v67, v234, v240, -v67
	v_fma_f32 v69, v234, v241, v69
	v_cvt_pk_f16_f32 v250, v66, v67
	v_cvt_pk_f16_f32 v252, v68, v69
	v_mfma_f32_32x32x16_f16 v[34:49], v[6:9], v[142:145], v[34:49]
	v_mul_f32_e32 v70, v237, v243
	v_mul_f32_e32 v72, v237, v242
	v_mul_f32_e32 v71, v237, v245
	v_mul_f32_e32 v73, v237, v244
	v_fma_f32 v70, v236, v242, -v70
	v_mfma_f32_32x32x16_f16 v[34:49], v[22:25], v[138:141], v[34:49]
	v_fma_f32 v72, v236, v243, v72
	v_fma_f32 v71, v236, v244, -v71
	v_fma_f32 v73, v236, v245, v73
	v_cvt_pk_f16_f32 v251, v70, v71
	v_cvt_pk_f16_f32 v253, v72, v73
	v_mfma_f32_32x32x16_f16 v[50:65], v[2:5], v[134:137], 0
	v_cvt_pk_f16_f32 v190, v190, v191
	v_cvt_pk_f16_f32 v191, v192, v193
	v_cvt_pk_f16_f32 v192, v194, v195
	v_cvt_pk_f16_f32 v193, v196, v197
	v_cvt_pk_f16_f32 v194, v198, v199
	v_mfma_f32_32x32x16_f16 v[50:65], v[18:21], v[126:129], v[50:65]
	v_cvt_pk_f16_f32 v195, v200, v201
	v_cvt_pk_f16_f32 v196, v202, v203
	v_cvt_pk_f16_f32 v197, v204, v205
	v_cvt_pk_f16_f32 v206, v206, v207
	v_cvt_pk_f16_f32 v207, v208, v209
	v_mfma_f32_32x32x16_f16 v[50:65], v[6:9], v[122:125], v[50:65]
	v_cvt_pk_f16_f32 v208, v210, v211
	v_cvt_pk_f16_f32 v209, v212, v213
	v_cvt_pk_f16_f32 v210, v214, v215
	v_cvt_pk_f16_f32 v211, v216, v217
	v_cvt_pk_f16_f32 v212, v218, v219
	v_mfma_f32_32x32x16_f16 v[50:65], v[22:25], v[130:133], v[50:65]
	v_cvt_pk_f16_f32 v213, v220, v221
	ds_write_b128 v173, v[190:193]
	ds_write_b128 v172, v[194:197]
	ds_write_b128 v173, v[206:209] offset:32768
	ds_write_b128 v172, v[210:213] offset:32768
	v_xor_b32_e32 v255, 24, v254
	ds_read2_b64 v[238:241], v255 offset0:0 offset1:16
	ds_read2_b64 v[242:245], v255 offset0:32 offset1:48
	v_mfma_f32_32x32x16_f16 v[2:17], v[222:225], v[246:249], 0
	v_mfma_f32_32x32x16_f16 v[18:33], v[226:229], v[250:253], 0
	v_cvt_pk_f16_f32 v34, v34, v35
	v_cvt_pk_f16_f32 v35, v36, v37
	v_cvt_pk_f16_f32 v36, v38, v39
	v_cvt_pk_f16_f32 v37, v40, v41
	v_cvt_pk_f16_f32 v38, v42, v43
	v_cvt_pk_f16_f32 v39, v44, v45
	v_cvt_pk_f16_f32 v40, v46, v47
	v_cvt_pk_f16_f32 v41, v48, v49
	v_cvt_pk_f16_f32 v50, v50, v51
	v_cvt_pk_f16_f32 v51, v52, v53
	v_cvt_pk_f16_f32 v52, v54, v55
	v_cvt_pk_f16_f32 v53, v56, v57
	v_cvt_pk_f16_f32 v54, v58, v59
	v_cvt_pk_f16_f32 v55, v60, v61
	v_cvt_pk_f16_f32 v56, v62, v63
	v_cvt_pk_f16_f32 v57, v64, v65
	v_mfma_f32_32x32x16_f16 v[190:205], v[34:37], v[118:121], 0
	v_cvt_pk_f16_f32 v2, v2, v3
	v_cvt_pk_f16_f32 v3, v4, v5
	v_cvt_pk_f16_f32 v4, v6, v7
	v_cvt_pk_f16_f32 v5, v8, v9
	v_mfma_f32_32x32x16_f16 v[206:221], v[34:37], v[102:105], 0
	v_cvt_pk_f16_f32 v6, v10, v11
	v_cvt_pk_f16_f32 v7, v12, v13
	v_cvt_pk_f16_f32 v8, v14, v15
	v_cvt_pk_f16_f32 v9, v16, v17
	v_cvt_pk_f16_f32 v18, v18, v19
	v_mfma_f32_32x32x16_f16 v[190:205], v[38:41], v[114:117], v[190:205]
	v_cvt_pk_f16_f32 v19, v20, v21
	v_cvt_pk_f16_f32 v20, v22, v23
	v_cvt_pk_f16_f32 v21, v24, v25
	v_cvt_pk_f16_f32 v22, v26, v27
	v_mfma_f32_32x32x16_f16 v[206:221], v[38:41], v[98:101], v[206:221]
	v_cvt_pk_f16_f32 v23, v28, v29
	v_cvt_pk_f16_f32 v24, v30, v31
	v_cvt_pk_f16_f32 v25, v32, v33
	s_waitcnt lgkmcnt(0)
	v_mul_f32_e32 v66, v231, v239
	v_mfma_f32_32x32x16_f16 v[190:205], v[50:53], v[110:113], v[190:205]
	v_mul_f32_e32 v68, v231, v238
	v_mul_f32_e32 v67, v231, v241
	v_mul_f32_e32 v69, v231, v240
	v_fma_f32 v66, v230, v238, -v66
	v_fma_f32 v68, v230, v239, v68
	v_mfma_f32_32x32x16_f16 v[206:221], v[50:53], v[94:97], v[206:221]
	v_fma_f32 v67, v230, v240, -v67
	v_fma_f32 v69, v230, v241, v69
	v_cvt_pk_f16_f32 v246, v66, v67
	v_cvt_pk_f16_f32 v248, v68, v69
	v_mfma_f32_32x32x16_f16 v[190:205], v[54:57], v[106:109], v[190:205]
	v_mul_f32_e32 v70, v233, v243
	v_mul_f32_e32 v72, v233, v242
	v_mul_f32_e32 v71, v233, v245
	v_mul_f32_e32 v73, v233, v244
	v_fma_f32 v70, v232, v242, -v70
	v_mfma_f32_32x32x16_f16 v[206:221], v[54:57], v[90:93], v[206:221]
	v_fma_f32 v72, v232, v243, v72
	v_fma_f32 v71, v232, v244, -v71
	v_fma_f32 v73, v232, v245, v73
	v_cvt_pk_f16_f32 v247, v70, v71
	v_cvt_pk_f16_f32 v249, v72, v73
	v_mfma_f32_32x32x16_f16 v[34:49], v[2:5], v[150:153], 0
	v_mul_f32_e32 v66, v235, v239
	v_mul_f32_e32 v68, v235, v238
	v_mul_f32_e32 v67, v235, v241
	v_mul_f32_e32 v69, v235, v240
	v_fma_f32 v66, v234, v238, -v66
	v_mfma_f32_32x32x16_f16 v[34:49], v[18:21], v[146:149], v[34:49]
	v_fma_f32 v68, v234, v239, v68
	v_fma_f32 v67, v234, v240, -v67
	v_fma_f32 v69, v234, v241, v69
	v_cvt_pk_f16_f32 v250, v66, v67
	v_cvt_pk_f16_f32 v252, v68, v69
	v_mfma_f32_32x32x16_f16 v[34:49], v[6:9], v[142:145], v[34:49]
	v_mul_f32_e32 v70, v237, v243
	v_mul_f32_e32 v72, v237, v242
	v_mul_f32_e32 v71, v237, v245
	v_mul_f32_e32 v73, v237, v244
	v_fma_f32 v70, v236, v242, -v70
	v_mfma_f32_32x32x16_f16 v[34:49], v[22:25], v[138:141], v[34:49]
	v_fma_f32 v72, v236, v243, v72
	v_fma_f32 v71, v236, v244, -v71
	v_fma_f32 v73, v236, v245, v73
	v_cvt_pk_f16_f32 v251, v70, v71
	v_cvt_pk_f16_f32 v253, v72, v73
	v_cvt_pk_f16_f32 v190, v190, v191
	v_mfma_f32_32x32x16_f16 v[50:65], v[2:5], v[134:137], 0
	v_cvt_pk_f16_f32 v191, v192, v193
	v_cvt_pk_f16_f32 v192, v194, v195
	v_cvt_pk_f16_f32 v193, v196, v197
	v_cvt_pk_f16_f32 v194, v198, v199
	v_cvt_pk_f16_f32 v195, v200, v201
	v_mfma_f32_32x32x16_f16 v[50:65], v[18:21], v[126:129], v[50:65]
	v_cvt_pk_f16_f32 v196, v202, v203
	v_cvt_pk_f16_f32 v197, v204, v205
	v_cvt_pk_f16_f32 v206, v206, v207
	v_cvt_pk_f16_f32 v207, v208, v209
	v_cvt_pk_f16_f32 v208, v210, v211
	v_mfma_f32_32x32x16_f16 v[50:65], v[6:9], v[122:125], v[50:65]
	v_cvt_pk_f16_f32 v209, v212, v213
	v_cvt_pk_f16_f32 v210, v214, v215
	v_cvt_pk_f16_f32 v211, v216, v217
	v_cvt_pk_f16_f32 v212, v218, v219
	v_cvt_pk_f16_f32 v213, v220, v221
	v_mfma_f32_32x32x16_f16 v[50:65], v[22:25], v[130:133], v[50:65]
	v_xor_b32_e32 v74, 0x8a0, v173
	v_xor_b32_e32 v75, 0x8a0, v172
	ds_write_b128 v74, v[190:193]
	ds_write_b128 v75, v[194:197]
	ds_write_b128 v74, v[206:209] offset:32768
	ds_write_b128 v75, v[210:213] offset:32768
	s_nop 0
	v_mfma_f32_32x32x16_f16 v[2:17], v[222:225], v[246:249], 0
	v_mfma_f32_32x32x16_f16 v[18:33], v[226:229], v[250:253], 0
	v_cvt_pk_f16_f32 v34, v34, v35
	v_cvt_pk_f16_f32 v35, v36, v37
	v_cvt_pk_f16_f32 v36, v38, v39
	v_cvt_pk_f16_f32 v37, v40, v41
	v_cvt_pk_f16_f32 v38, v42, v43
	v_cvt_pk_f16_f32 v39, v44, v45
	v_cvt_pk_f16_f32 v40, v46, v47
	v_cvt_pk_f16_f32 v41, v48, v49
	v_cvt_pk_f16_f32 v50, v50, v51
	v_cvt_pk_f16_f32 v51, v52, v53
	v_cvt_pk_f16_f32 v52, v54, v55
	v_cvt_pk_f16_f32 v53, v56, v57
	v_cvt_pk_f16_f32 v54, v58, v59
	v_cvt_pk_f16_f32 v55, v60, v61
	v_cvt_pk_f16_f32 v56, v62, v63
	v_cvt_pk_f16_f32 v57, v64, v65
	v_mfma_f32_32x32x16_f16 v[190:205], v[34:37], v[118:121], 0
	v_cvt_pk_f16_f32 v2, v2, v3
	v_cvt_pk_f16_f32 v3, v4, v5
	v_mfma_f32_32x32x16_f16 v[206:221], v[34:37], v[102:105], 0
	v_cvt_pk_f16_f32 v4, v6, v7
	v_cvt_pk_f16_f32 v5, v8, v9
	v_mfma_f32_32x32x16_f16 v[190:205], v[38:41], v[114:117], v[190:205]
	v_cvt_pk_f16_f32 v6, v10, v11
	v_cvt_pk_f16_f32 v7, v12, v13
	v_mfma_f32_32x32x16_f16 v[206:221], v[38:41], v[98:101], v[206:221]
	v_cvt_pk_f16_f32 v8, v14, v15
	v_cvt_pk_f16_f32 v9, v16, v17
	v_mfma_f32_32x32x16_f16 v[190:205], v[50:53], v[110:113], v[190:205]
	v_cvt_pk_f16_f32 v18, v18, v19
	v_cvt_pk_f16_f32 v19, v20, v21
	v_mfma_f32_32x32x16_f16 v[206:221], v[50:53], v[94:97], v[206:221]
	v_cvt_pk_f16_f32 v20, v22, v23
	v_cvt_pk_f16_f32 v21, v24, v25
	v_mfma_f32_32x32x16_f16 v[190:205], v[54:57], v[106:109], v[190:205]
	v_cvt_pk_f16_f32 v22, v26, v27
	v_cvt_pk_f16_f32 v23, v28, v29
	v_mfma_f32_32x32x16_f16 v[206:221], v[54:57], v[90:93], v[206:221]
	v_cvt_pk_f16_f32 v24, v30, v31
	v_cvt_pk_f16_f32 v25, v32, v33
	v_mfma_f32_32x32x16_f16 v[34:49], v[2:5], v[150:153], 0
	v_mfma_f32_32x32x16_f16 v[34:49], v[18:21], v[146:149], v[34:49]
	v_mfma_f32_32x32x16_f16 v[34:49], v[6:9], v[142:145], v[34:49]
	v_mfma_f32_32x32x16_f16 v[34:49], v[22:25], v[138:141], v[34:49]
	v_mfma_f32_32x32x16_f16 v[50:65], v[2:5], v[134:137], 0
	s_nop 5
	v_cvt_pk_f16_f32 v190, v190, v191
	v_cvt_pk_f16_f32 v191, v192, v193
	v_cvt_pk_f16_f32 v192, v194, v195
	v_cvt_pk_f16_f32 v193, v196, v197
	v_mfma_f32_32x32x16_f16 v[50:65], v[18:21], v[126:129], v[50:65]
	v_cvt_pk_f16_f32 v194, v198, v199
	v_cvt_pk_f16_f32 v195, v200, v201
	v_cvt_pk_f16_f32 v196, v202, v203
	v_cvt_pk_f16_f32 v197, v204, v205
	v_cvt_pk_f16_f32 v206, v206, v207
	v_cvt_pk_f16_f32 v207, v208, v209
	v_mfma_f32_32x32x16_f16 v[50:65], v[6:9], v[122:125], v[50:65]
	v_cvt_pk_f16_f32 v208, v210, v211
	v_cvt_pk_f16_f32 v209, v212, v213
	v_cvt_pk_f16_f32 v210, v214, v215
	v_cvt_pk_f16_f32 v211, v216, v217
	v_cvt_pk_f16_f32 v212, v218, v219
	v_cvt_pk_f16_f32 v213, v220, v221
	v_mfma_f32_32x32x16_f16 v[50:65], v[22:25], v[130:133], v[50:65]
	v_xor_b32_e32 v74, 0x1040, v173
	v_xor_b32_e32 v75, 0x1040, v172
	ds_write_b128 v74, v[190:193]
	ds_write_b128 v75, v[194:197]
	ds_write_b128 v74, v[206:209] offset:32768
	ds_write_b128 v75, v[210:213] offset:32768
	s_nop 11
	v_cvt_pk_f16_f32 v34, v34, v35
	v_cvt_pk_f16_f32 v35, v36, v37
	v_cvt_pk_f16_f32 v36, v38, v39
	v_cvt_pk_f16_f32 v37, v40, v41
	v_cvt_pk_f16_f32 v38, v42, v43
	v_cvt_pk_f16_f32 v39, v44, v45
	v_cvt_pk_f16_f32 v40, v46, v47
	v_cvt_pk_f16_f32 v41, v48, v49
	v_cvt_pk_f16_f32 v50, v50, v51
	v_cvt_pk_f16_f32 v51, v52, v53
	v_cvt_pk_f16_f32 v52, v54, v55
	v_cvt_pk_f16_f32 v53, v56, v57
	v_cvt_pk_f16_f32 v54, v58, v59
	v_cvt_pk_f16_f32 v55, v60, v61
	v_cvt_pk_f16_f32 v56, v62, v63
	v_cvt_pk_f16_f32 v57, v64, v65
	v_mfma_f32_32x32x16_f16 v[190:205], v[34:37], v[118:121], 0
	v_mfma_f32_32x32x16_f16 v[206:221], v[34:37], v[102:105], 0
	v_mfma_f32_32x32x16_f16 v[190:205], v[38:41], v[114:117], v[190:205]
	v_mfma_f32_32x32x16_f16 v[206:221], v[38:41], v[98:101], v[206:221]
	v_mfma_f32_32x32x16_f16 v[190:205], v[50:53], v[110:113], v[190:205]
	v_mfma_f32_32x32x16_f16 v[206:221], v[50:53], v[94:97], v[206:221]
	v_mfma_f32_32x32x16_f16 v[190:205], v[54:57], v[106:109], v[190:205]
	v_mfma_f32_32x32x16_f16 v[206:221], v[54:57], v[90:93], v[206:221]
	v_and_b32_e32 v134, 1, v156
	v_bitop3_b32 v132, v171, s40, v170 bitop3:0x36
	v_bitop3_b32 v131, s41, v154, v160 bitop3:0x36
	v_bitop3_b32 v135, v171, s42, v170 bitop3:0x36
	v_xor_b32_e32 v133, s43, v154
	v_and_b32_e32 v130, 4, v156
	s_lshl_b32 s2, s27, 3
	s_lshl_b32 s3, s5, 2
	s_or_b32 s2, s3, s2
	s_ashr_i32 s3, s2, 31
	s_lshl_b64 s[2:3], s[2:3], 13
	s_add_u32 s2, s20, s2
	s_addc_u32 s3, s21, s3
	v_lshlrev_b32_e32 v154, 1, v169
	v_lshl_add_u64 v[2:3], s[2:3], 0, v[154:155]
	v_add_co_u32_e32 v2, vcc, s23, v2
	s_nop 1
	v_addc_co_u32_e32 v3, vcc, 0, v3, vcc
	v_cvt_pk_f16_f32 v190, v190, v191
	v_cvt_pk_f16_f32 v191, v192, v193
	v_cvt_pk_f16_f32 v192, v194, v195
	v_cvt_pk_f16_f32 v193, v196, v197
	v_cvt_pk_f16_f32 v194, v198, v199
	v_cvt_pk_f16_f32 v195, v200, v201
	v_cvt_pk_f16_f32 v196, v202, v203
	v_cvt_pk_f16_f32 v197, v204, v205
	v_cvt_pk_f16_f32 v206, v206, v207
	v_cvt_pk_f16_f32 v207, v208, v209
	v_cvt_pk_f16_f32 v208, v210, v211
	v_cvt_pk_f16_f32 v209, v212, v213
	v_cvt_pk_f16_f32 v210, v214, v215
	v_cvt_pk_f16_f32 v211, v216, v217
	v_cvt_pk_f16_f32 v212, v218, v219
	v_cvt_pk_f16_f32 v213, v220, v221
	v_xor_b32_e32 v74, 0x18e0, v173
	v_xor_b32_e32 v75, 0x18e0, v172
	ds_write_b128 v74, v[190:193]
	ds_write_b128 v75, v[194:197]
	ds_write_b128 v74, v[206:209] offset:32768
	ds_write_b128 v75, v[210:213] offset:32768
	s_setprio 0
	s_waitcnt lgkmcnt(0)
	s_barrier
	global_load_dwordx4 v[62:65], v154, s[2:3]
	global_load_dwordx4 v[46:49], v154, s[2:3] offset:1024
	global_load_dwordx4 v[42:45], v154, s[2:3] offset:2048
	global_load_dwordx4 v[38:41], v154, s[2:3] offset:3072
	global_load_dwordx4 v[54:57], v[2:3], off offset:1024
	global_load_dwordx4 v[50:53], v[2:3], off offset:2048
	v_lshl_add_u64 v[4:5], s[12:13], 0, v[154:155]
	global_load_dwordx4 v[126:129], v154, s[12:13]
	global_load_dwordx4 v[122:125], v154, s[12:13] offset:1024
	global_load_dwordx4 v[118:121], v154, s[12:13] offset:2048
	global_load_dwordx4 v[114:117], v154, s[12:13] offset:3072
	global_load_dwordx4 v[34:37], v168, s[2:3]
	global_load_dwordx4 v[110:113], v168, s[12:13]
	v_add_co_u32_e32 v4, vcc, s23, v4
	s_nop 1
	v_addc_co_u32_e32 v5, vcc, 0, v5, vcc
	global_load_dwordx4 v[58:61], v[2:3], off offset:3072
	global_load_dwordx4 v[106:109], v[4:5], off offset:1024
	global_load_dwordx4 v[94:97], v[4:5], off offset:2048
	global_load_dwordx4 v[90:93], v[4:5], off offset:3072
	v_bfrev_b32_e32 v3, v156
	v_lshlrev_b32_e32 v7, 5, v167
	v_lshlrev_b32_e32 v6, 9, v167
	v_and_b32_e32 v7, 0x200, v7
	v_lshlrev_b32_e32 v8, 8, v167
	v_lshrrev_b32_e32 v3, 27, v3
	v_lshrrev_b32_e32 v2, 2, v167
	v_lshrrev_b32_e32 v4, 4, v156
	v_xor_b32_e32 v5, v169, v156
	v_and_b32_e32 v6, 0x5800, v6
	v_and_b32_e32 v3, 8, v3
	v_and_or_b32 v7, v8, s24, v7
	v_lshrrev_b32_e32 v5, 1, v5
	v_xor_b32_e32 v4, v2, v4
	v_or3_b32 v3, v7, v6, v3
	v_bitop3_b32 v7, v2, v182, 1 bitop3:0x6c
	v_lshlrev_b32_e32 v2, 1, v167
	v_and_b32_e32 v5, 4, v5
	v_lshlrev_b32_e32 v4, 3, v4
	v_lshrrev_b32_e32 v6, 1, v167
	v_and_b32_e32 v2, 2, v2
	v_and_or_b32 v9, v169, 8, v2
	v_and_b32_e32 v2, 8, v4
	v_and_or_b32 v4, v6, 2, v5
	v_or3_b32 v2, v4, v2, v134
	v_lshlrev_b32_e32 v2, 4, v2
	v_bitop3_b32 v146, v3, s28, v2 bitop3:0x36
	v_xor_b32_e32 v8, v6, v182
	v_xor_b32_e32 v147, 0x2010, v146
	v_lshlrev_b32_e32 v8, 2, v8
	v_and_b32_e32 v8, 4, v8
	v_or3_b32 v6, v9, v7, v8
	v_lshlrev_b32_e32 v7, 11, v167
	v_and_b32_e32 v8, 0x7800, v7
	v_lshlrev_b32_e32 v6, 4, v6
	v_or3_b32 v22, v6, v8, v170
	v_and_b32_e32 v23, 0x8000, v7
	v_xor_b32_e32 v150, 16, v146
	v_xad_u32 v70, v22, s28, v23
	v_xor_b32_e32 v151, 0x2000, v146
	ds_read_b64_tr_b16 v[18:19], v146
	ds_read_b64_tr_b16 v[20:21], v147
	ds_read_b64_tr_b16 v[22:23], v146 offset:32768
	ds_read_b64_tr_b16 v[24:25], v147 offset:32768
	ds_read_b64_tr_b16 v[26:27], v150
	ds_read_b64_tr_b16 v[28:29], v151
	ds_read_b64_tr_b16 v[30:31], v150 offset:32768
	ds_read_b64_tr_b16 v[32:33], v151 offset:32768
	v_xor_b32_e32 v148, 32, v146
	v_xor_b32_e32 v149, 0x2030, v146
	v_xor_b32_e32 v144, 48, v146
	v_xor_b32_e32 v145, 0x2020, v146
	v_xor_b32_e32 v142, 64, v146
	v_xor_b32_e32 v143, 0x2050, v146
	v_xor_b32_e32 v140, 0x50, v146
	v_xor_b32_e32 v141, 0x2040, v146
	v_xor_b32_e32 v138, 0x60, v146
	v_xor_b32_e32 v139, 0x2070, v146
	v_xor_b32_e32 v136, 0x70, v146
	v_xor_b32_e32 v137, 0x2060, v146
	v_xor_b32_e32 v71, 0x60, v70
	s_lshl_b64 s[0:1], s[0:1], 13
	s_add_u32 s0, s8, s0
	s_addc_u32 s1, s9, s1
	s_waitcnt vmcnt(17) lgkmcnt(4)
	v_mfma_f32_32x32x16_f16 v[2:17], v[18:21], v[86:89], 0
	s_waitcnt vmcnt(16)
	v_mfma_f32_32x32x16_f16 v[2:17], v[22:25], v[82:85], v[2:17]
	ds_read_b64_tr_b16 v[206:207], v148
	ds_read_b64_tr_b16 v[208:209], v149
	ds_read_b64_tr_b16 v[210:211], v148 offset:32768
	ds_read_b64_tr_b16 v[212:213], v149 offset:32768
	s_waitcnt lgkmcnt(4)
	v_mfma_f32_32x32x16_f16 v[190:205], v[26:29], v[86:89], 0
	v_mfma_f32_32x32x16_f16 v[190:205], v[30:33], v[82:85], v[190:205]
	s_nop 4
	v_cvt_pk_f16_f32 v2, v2, v3
	v_cvt_pk_f16_f32 v3, v4, v5
	v_cvt_pk_f16_f32 v4, v6, v7
	v_cvt_pk_f16_f32 v5, v8, v9
	v_cvt_pk_f16_f32 v6, v10, v11
	v_cvt_pk_f16_f32 v7, v12, v13
	v_cvt_pk_f16_f32 v8, v14, v15
	v_cvt_pk_f16_f32 v9, v16, v17
	v_xor_b32_e32 v73, 0x280, v70
	ds_write_b128 v70, v[2:5]
	ds_write_b128 v73, v[6:9]
	ds_read_b64_tr_b16 v[18:19], v144
	ds_read_b64_tr_b16 v[20:21], v145
	ds_read_b64_tr_b16 v[22:23], v144 offset:32768
	ds_read_b64_tr_b16 v[24:25], v145 offset:32768
	s_waitcnt lgkmcnt(6)
	v_mfma_f32_32x32x16_f16 v[2:17], v[206:209], v[86:89], 0
	v_mfma_f32_32x32x16_f16 v[2:17], v[210:213], v[82:85], v[2:17]
	v_cvt_pk_f16_f32 v190, v190, v191
	v_cvt_pk_f16_f32 v191, v192, v193
	v_cvt_pk_f16_f32 v192, v194, v195
	v_cvt_pk_f16_f32 v193, v196, v197
	v_cvt_pk_f16_f32 v194, v198, v199
	v_cvt_pk_f16_f32 v195, v200, v201
	v_cvt_pk_f16_f32 v196, v202, v203
	v_cvt_pk_f16_f32 v197, v204, v205
	v_xor_b32_e32 v72, 16, v70
	v_xor_b32_e32 v73, 0x290, v70
	ds_write_b128 v72, v[190:193]
	ds_write_b128 v73, v[194:197]
	ds_read_b64_tr_b16 v[26:27], v142
	ds_read_b64_tr_b16 v[28:29], v143
	ds_read_b64_tr_b16 v[30:31], v142 offset:32768
	ds_read_b64_tr_b16 v[32:33], v143 offset:32768
	s_waitcnt lgkmcnt(6)
	v_mfma_f32_32x32x16_f16 v[190:205], v[18:21], v[86:89], 0
	v_mfma_f32_32x32x16_f16 v[190:205], v[22:25], v[82:85], v[190:205]
	v_cvt_pk_f16_f32 v2, v2, v3
	v_cvt_pk_f16_f32 v3, v4, v5
	v_cvt_pk_f16_f32 v4, v6, v7
	v_cvt_pk_f16_f32 v5, v8, v9
	v_cvt_pk_f16_f32 v6, v10, v11
	v_cvt_pk_f16_f32 v7, v12, v13
	v_cvt_pk_f16_f32 v8, v14, v15
	v_cvt_pk_f16_f32 v9, v16, v17
	v_xor_b32_e32 v72, 32, v70
	v_xor_b32_e32 v73, 0x2a0, v70
	ds_write_b128 v72, v[2:5]
	ds_write_b128 v73, v[6:9]
	ds_read_b64_tr_b16 v[206:207], v140
	ds_read_b64_tr_b16 v[208:209], v141
	ds_read_b64_tr_b16 v[210:211], v140 offset:32768
	ds_read_b64_tr_b16 v[212:213], v141 offset:32768
	s_waitcnt lgkmcnt(6)
	v_mfma_f32_32x32x16_f16 v[2:17], v[26:29], v[86:89], 0
	v_mfma_f32_32x32x16_f16 v[2:17], v[30:33], v[82:85], v[2:17]
	v_cvt_pk_f16_f32 v190, v190, v191
	v_cvt_pk_f16_f32 v191, v192, v193
	v_cvt_pk_f16_f32 v192, v194, v195
	v_cvt_pk_f16_f32 v193, v196, v197
	v_cvt_pk_f16_f32 v194, v198, v199
	v_cvt_pk_f16_f32 v195, v200, v201
	v_cvt_pk_f16_f32 v196, v202, v203
	v_cvt_pk_f16_f32 v197, v204, v205
	v_xor_b32_e32 v72, 48, v70
	v_xor_b32_e32 v73, 0x2b0, v70
	ds_write_b128 v72, v[190:193]
	ds_write_b128 v73, v[194:197]
	ds_read_b64_tr_b16 v[18:19], v138
	ds_read_b64_tr_b16 v[20:21], v139
	ds_read_b64_tr_b16 v[22:23], v138 offset:32768
	ds_read_b64_tr_b16 v[24:25], v139 offset:32768
	s_waitcnt lgkmcnt(6)
	v_mfma_f32_32x32x16_f16 v[190:205], v[206:209], v[86:89], 0
	v_mfma_f32_32x32x16_f16 v[190:205], v[210:213], v[82:85], v[190:205]
	v_cvt_pk_f16_f32 v2, v2, v3
	v_cvt_pk_f16_f32 v3, v4, v5
	v_cvt_pk_f16_f32 v4, v6, v7
	v_cvt_pk_f16_f32 v5, v8, v9
	v_cvt_pk_f16_f32 v6, v10, v11
	v_cvt_pk_f16_f32 v7, v12, v13
	v_cvt_pk_f16_f32 v8, v14, v15
	v_cvt_pk_f16_f32 v9, v16, v17
	v_xor_b32_e32 v72, 64, v70
	v_xor_b32_e32 v73, 0x2c0, v70
	ds_write_b128 v72, v[2:5]
	ds_write_b128 v73, v[6:9]
	ds_read_b64_tr_b16 v[26:27], v136
	ds_read_b64_tr_b16 v[28:29], v137
	ds_read_b64_tr_b16 v[30:31], v136 offset:32768
	ds_read_b64_tr_b16 v[32:33], v137 offset:32768
	s_waitcnt lgkmcnt(6)
	v_mfma_f32_32x32x16_f16 v[2:17], v[18:21], v[86:89], 0
	v_mfma_f32_32x32x16_f16 v[2:17], v[22:25], v[82:85], v[2:17]
	v_cvt_pk_f16_f32 v190, v190, v191
	v_cvt_pk_f16_f32 v191, v192, v193
	v_cvt_pk_f16_f32 v192, v194, v195
	v_cvt_pk_f16_f32 v193, v196, v197
	v_cvt_pk_f16_f32 v194, v198, v199
	v_cvt_pk_f16_f32 v195, v200, v201
	v_cvt_pk_f16_f32 v196, v202, v203
	v_cvt_pk_f16_f32 v197, v204, v205
	v_xor_b32_e32 v72, 0x50, v70
	v_xor_b32_e32 v73, 0x2d0, v70
	ds_write_b128 v72, v[190:193]
	ds_write_b128 v73, v[194:197]
	s_waitcnt lgkmcnt(2)
	v_mfma_f32_32x32x16_f16 v[190:205], v[26:29], v[86:89], 0
	v_mfma_f32_32x32x16_f16 v[190:205], v[30:33], v[82:85], v[190:205]
	v_cvt_pk_f16_f32 v2, v2, v3
	v_cvt_pk_f16_f32 v3, v4, v5
	v_cvt_pk_f16_f32 v4, v6, v7
	v_cvt_pk_f16_f32 v5, v8, v9
	v_cvt_pk_f16_f32 v6, v10, v11
	v_cvt_pk_f16_f32 v7, v12, v13
	v_cvt_pk_f16_f32 v8, v14, v15
	v_cvt_pk_f16_f32 v9, v16, v17
	v_xor_b32_e32 v72, 0x60, v70
	v_xor_b32_e32 v73, 0x2e0, v70
	ds_write_b128 v72, v[2:5]
	ds_write_b128 v73, v[6:9]
	v_cvt_pk_f16_f32 v190, v190, v191
	v_cvt_pk_f16_f32 v191, v192, v193
	v_cvt_pk_f16_f32 v192, v194, v195
	v_cvt_pk_f16_f32 v193, v196, v197
	v_cvt_pk_f16_f32 v194, v198, v199
	v_cvt_pk_f16_f32 v195, v200, v201
	v_cvt_pk_f16_f32 v196, v202, v203
	v_cvt_pk_f16_f32 v197, v204, v205
	v_xor_b32_e32 v72, 0x70, v70
	v_xor_b32_e32 v73, 0x2f0, v70
	ds_write_b128 v72, v[190:193]
	ds_write_b128 v73, v[194:197]
	v_lshl_add_u64 v[2:3], s[0:1], 0, v[154:155]
	v_lshl_add_u64 v[4:5], v[2:3], 0, s[18:19]
	v_add_co_u32_e32 v2, vcc, s25, v2
	s_waitcnt lgkmcnt(0)
	s_nop 0
	v_addc_co_u32_e32 v3, vcc, 0, v3, vcc
	s_barrier
	s_nop 0
	s_nop 0
	global_load_dwordx4 v[102:105], v[2:3], off
	global_load_dwordx4 v[98:101], v[4:5], off offset:1024
	s_setprio 1
	s_add_u32 s0, s2, 0x2000
	s_addc_u32 s1, s3, 0
	v_lshl_add_u64 v[2:3], s[0:1], 0, v[154:155]
	v_add_co_u32_e32 v2, vcc, s23, v2
	global_load_dwordx4 v[66:69], v154, s[0:1]
	global_load_dwordx4 v[70:73], v154, s[0:1] offset:1024
	global_load_dwordx4 v[74:77], v154, s[0:1] offset:2048
	global_load_dwordx4 v[78:81], v154, s[0:1] offset:3072
	v_addc_co_u32_e32 v3, vcc, 0, v3, vcc
	global_load_dwordx4 v[82:85], v168, s[0:1]
	global_load_dwordx4 v[86:89], v[2:3], off offset:1024
	global_load_dwordx4 v[182:185], v[2:3], off offset:2048
	global_load_dwordx4 v[186:189], v[2:3], off offset:3072
	ds_read_b128 v[18:21], v179
	ds_read_b128 v[22:25], v179 offset:32768
	ds_read_b128 v[26:29], v178
	ds_read_b128 v[30:33], v178 offset:32768
	s_add_u32 s0, s2, 0x6000
	s_addc_u32 s1, s3, 0
	s_waitcnt vmcnt(25) lgkmcnt(3)
	v_mfma_f32_32x32x16_f16 v[2:17], v[18:21], v[62:65], 0
	s_add_u32 s2, s2, 0x4000
	s_addc_u32 s3, s3, 0
	s_or_b32 s27, s26, 0x8a0
	s_or_b32 s26, s26, 0xa20
	s_waitcnt vmcnt(24) lgkmcnt(1)
	v_mfma_f32_32x32x16_f16 v[2:17], v[26:29], v[46:49], v[2:17]
	s_waitcnt vmcnt(23)
	v_mfma_f32_32x32x16_f16 v[2:17], v[22:25], v[42:45], v[2:17]
	s_waitcnt vmcnt(22) lgkmcnt(0)
	v_mfma_f32_32x32x16_f16 v[2:17], v[30:33], v[38:41], v[2:17]
	s_waitcnt vmcnt(15)
	v_mfma_f32_32x32x16_f16 v[34:49], v[18:21], v[34:37], 0
	s_nop 9
	v_cvt_pk_f16_f32 v9, v8, v9
	v_cvt_pk_f16_f32 v8, v6, v7
	v_cvt_pk_f16_f32 v7, v4, v5
	v_cvt_pk_f16_f32 v6, v2, v3
	v_cvt_pk_f16_f32 v5, v16, v17
	v_cvt_pk_f16_f32 v4, v14, v15
	v_cvt_pk_f16_f32 v3, v12, v13
	v_mfma_f32_32x32x16_f16 v[34:49], v[26:29], v[54:57], v[34:49]
	v_cvt_pk_f16_f32 v2, v10, v11
	v_mfma_f32_32x32x16_f16 v[34:49], v[22:25], v[50:53], v[34:49]
	s_waitcnt vmcnt(13)
	v_mfma_f32_32x32x16_f16 v[34:49], v[30:33], v[58:61], v[34:49]
	v_mfma_f32_32x32x16_f16 v[18:33], v[6:9], v[126:129], 0
	s_nop 10
	v_cvt_pk_f16_f32 v13, v40, v41
	v_cvt_pk_f16_f32 v12, v38, v39
	v_cvt_pk_f16_f32 v11, v36, v37
	v_cvt_pk_f16_f32 v10, v34, v35
	v_cvt_pk_f16_f32 v17, v48, v49
	v_cvt_pk_f16_f32 v16, v46, v47
	v_cvt_pk_f16_f32 v15, v44, v45
	v_mfma_f32_32x32x16_f16 v[50:65], v[6:9], v[110:113], 0
	v_bitop3_b32 v6, v171, s27, v170 bitop3:0x36
	v_cvt_pk_f16_f32 v14, v42, v43
	v_mfma_f32_32x32x16_f16 v[18:33], v[2:5], v[122:125], v[18:33]
	s_waitcnt vmcnt(12)
	v_mfma_f32_32x32x16_f16 v[50:65], v[2:5], v[106:109], v[50:65]
	ds_read_b128 v[2:5], v6
	ds_read_b128 v[6:9], v6 offset:32768
	v_mfma_f32_32x32x16_f16 v[18:33], v[10:13], v[118:121], v[18:33]
	s_waitcnt vmcnt(11)
	v_mfma_f32_32x32x16_f16 v[50:65], v[10:13], v[94:97], v[50:65]
	s_waitcnt vmcnt(7) lgkmcnt(1)
	v_mfma_f32_32x32x16_f16 v[34:49], v[2:5], v[66:69], 0
	v_mfma_f32_32x32x16_f16 v[18:33], v[14:17], v[114:117], v[18:33]
	v_mfma_f32_32x32x16_f16 v[50:65], v[14:17], v[90:93], v[50:65]
	v_bitop3_b32 v14, v171, s26, v170 bitop3:0x36
	ds_read_b128 v[10:13], v14
	ds_read_b128 v[14:17], v14 offset:32768
	s_nop 7
	v_cvt_pk_f16_f32 v25, v24, v25
	v_cvt_pk_f16_f32 v24, v22, v23
	v_cvt_pk_f16_f32 v23, v20, v21
	v_cvt_pk_f16_f32 v22, v18, v19
	v_cvt_pk_f16_f32 v21, v32, v33
	s_waitcnt vmcnt(6) lgkmcnt(1)
	v_mfma_f32_32x32x16_f16 v[34:49], v[10:13], v[70:73], v[34:49]
	v_cvt_pk_f16_f32 v20, v30, v31
	v_cvt_pk_f16_f32 v19, v28, v29
	v_cvt_pk_f16_f32 v18, v26, v27
	ds_write_b128 v173, v[22:25]
	ds_write_b128 v172, v[18:21]
	v_cvt_pk_f16_f32 v21, v56, v57
	v_cvt_pk_f16_f32 v20, v54, v55
	s_waitcnt vmcnt(5)
	v_mfma_f32_32x32x16_f16 v[34:49], v[6:9], v[74:77], v[34:49]
	v_cvt_pk_f16_f32 v19, v52, v53
	v_cvt_pk_f16_f32 v18, v50, v51
	ds_write_b128 v173, v[18:21] offset:32768
	v_cvt_pk_f16_f32 v21, v64, v65
	v_cvt_pk_f16_f32 v20, v62, v63
	v_cvt_pk_f16_f32 v19, v60, v61
	v_cvt_pk_f16_f32 v18, v58, v59
	s_waitcnt vmcnt(4) lgkmcnt(3)
	v_mfma_f32_32x32x16_f16 v[34:49], v[14:17], v[78:81], v[34:49]
	ds_write_b128 v172, v[18:21] offset:32768
	s_waitcnt vmcnt(3)
	v_mfma_f32_32x32x16_f16 v[66:81], v[2:5], v[82:85], 0
	s_nop 8
	v_cvt_pk_f16_f32 v41, v40, v41
	v_cvt_pk_f16_f32 v40, v38, v39
	v_cvt_pk_f16_f32 v39, v36, v37
	v_cvt_pk_f16_f32 v38, v34, v35
	v_cvt_pk_f16_f32 v85, v48, v49
	v_cvt_pk_f16_f32 v84, v46, v47
	v_cvt_pk_f16_f32 v83, v44, v45
	s_waitcnt vmcnt(2)
	v_mfma_f32_32x32x16_f16 v[66:81], v[10:13], v[86:89], v[66:81]
	v_cvt_pk_f16_f32 v82, v42, v43
	s_waitcnt vmcnt(1)
	v_mfma_f32_32x32x16_f16 v[66:81], v[6:9], v[182:185], v[66:81]
	s_waitcnt vmcnt(0)
	v_mfma_f32_32x32x16_f16 v[66:81], v[14:17], v[186:189], v[66:81]
	v_mfma_f32_32x32x16_f16 v[2:17], v[38:41], v[126:129], 0
	s_nop 10
	v_cvt_pk_f16_f32 v73, v72, v73
	v_cvt_pk_f16_f32 v72, v70, v71
	v_cvt_pk_f16_f32 v70, v66, v67
	v_cvt_pk_f16_f32 v67, v76, v77
	v_cvt_pk_f16_f32 v66, v74, v75
	global_load_dwordx4 v[74:77], v154, s[2:3]
	v_cvt_pk_f16_f32 v71, v68, v69
	v_cvt_pk_f16_f32 v69, v80, v81
	v_cvt_pk_f16_f32 v68, v78, v79
	global_load_dwordx4 v[78:81], v154, s[2:3] offset:1024
	ds_read_b128 v[18:21], v180
	ds_read_b128 v[22:25], v176
	ds_read_b128 v[26:29], v180 offset:32768
	global_load_dwordx4 v[30:33], v154, s[2:3] offset:2048
	v_mfma_f32_32x32x16_f16 v[34:49], v[38:41], v[110:113], 0
	v_mfma_f32_32x32x16_f16 v[2:17], v[82:85], v[122:125], v[2:17]
	v_mfma_f32_32x32x16_f16 v[34:49], v[82:85], v[106:109], v[34:49]
	ds_read_b128 v[82:85], v176 offset:32768
	s_waitcnt vmcnt(2) lgkmcnt(3)
	v_mfma_f32_32x32x16_f16 v[50:65], v[18:21], v[74:77], 0
	v_mfma_f32_32x32x16_f16 v[2:17], v[70:73], v[118:121], v[2:17]
	v_mfma_f32_32x32x16_f16 v[34:49], v[70:73], v[94:97], v[34:49]
	v_lshl_add_u64 v[70:71], s[2:3], 0, v[154:155]
	v_add_co_u32_e32 v152, vcc, s23, v70
	s_nop 1
	v_addc_co_u32_e32 v153, vcc, 0, v71, vcc
	s_waitcnt vmcnt(1) lgkmcnt(2)
	v_mfma_f32_32x32x16_f16 v[50:65], v[22:25], v[78:81], v[50:65]
	v_mfma_f32_32x32x16_f16 v[2:17], v[66:69], v[114:117], v[2:17]
	v_mfma_f32_32x32x16_f16 v[34:49], v[66:69], v[90:93], v[34:49]
	global_load_dwordx4 v[66:69], v154, s[2:3] offset:3072
	s_nop 9
	v_cvt_pk_f16_f32 v9, v8, v9
	v_cvt_pk_f16_f32 v8, v6, v7
	v_cvt_pk_f16_f32 v7, v4, v5
	v_cvt_pk_f16_f32 v6, v2, v3
	v_cvt_pk_f16_f32 v5, v16, v17
	v_cvt_pk_f16_f32 v4, v14, v15
	s_waitcnt vmcnt(1) lgkmcnt(1)
	v_mfma_f32_32x32x16_f16 v[50:65], v[26:29], v[30:33], v[50:65]
	global_load_dwordx4 v[30:33], v168, s[2:3]
	global_load_dwordx4 v[86:89], v[152:153], off offset:1024
	s_nop 0
	global_load_dwordx4 v[168:171], v168, s[0:1]
	v_cvt_pk_f16_f32 v3, v12, v13
	v_cvt_pk_f16_f32 v2, v10, v11
	ds_write_b128 v175, v[6:9]
	ds_write_b128 v174, v[2:5]
	v_cvt_pk_f16_f32 v5, v40, v41
	s_waitcnt vmcnt(3) lgkmcnt(2)
	v_mfma_f32_32x32x16_f16 v[50:65], v[82:85], v[66:69], v[50:65]
	global_load_dwordx4 v[182:185], v154, s[0:1] offset:1024
	v_cvt_pk_f16_f32 v4, v38, v39
	v_cvt_pk_f16_f32 v3, v36, v37
	v_cvt_pk_f16_f32 v2, v34, v35
	ds_write_b128 v175, v[2:5] offset:32768
	v_cvt_pk_f16_f32 v5, v48, v49
	v_cvt_pk_f16_f32 v4, v46, v47
	s_waitcnt vmcnt(3)
	v_mfma_f32_32x32x16_f16 v[66:81], v[18:21], v[30:33], 0
	global_load_dwordx4 v[18:21], v[152:153], off offset:2048
	v_cvt_pk_f16_f32 v3, v44, v45
	v_cvt_pk_f16_f32 v2, v42, v43
	ds_write_b128 v174, v[2:5] offset:32768
	v_cvt_pk_f16_f32 v57, v56, v57
	v_cvt_pk_f16_f32 v56, v54, v55
	v_cvt_pk_f16_f32 v55, v52, v53
	s_waitcnt vmcnt(3)
	v_mfma_f32_32x32x16_f16 v[66:81], v[22:25], v[86:89], v[66:81]
	global_load_dwordx4 v[22:25], v[152:153], off offset:3072
	v_cvt_pk_f16_f32 v54, v50, v51
	s_waitcnt vmcnt(1)
	v_mfma_f32_32x32x16_f16 v[66:81], v[26:29], v[18:21], v[66:81]
	v_lshl_add_u64 v[18:19], s[0:1], 0, v[154:155]
	v_add_co_u32_e32 v152, vcc, s23, v18
	s_nop 1
	v_addc_co_u32_e32 v153, vcc, 0, v19, vcc
	global_load_dwordx4 v[86:89], v[152:153], off offset:1024
	s_waitcnt vmcnt(1)
	v_mfma_f32_32x32x16_f16 v[66:81], v[82:85], v[22:25], v[66:81]
	v_cvt_pk_f16_f32 v85, v64, v65
	v_cvt_pk_f16_f32 v84, v62, v63
	v_cvt_pk_f16_f32 v83, v60, v61
	v_cvt_pk_f16_f32 v82, v58, v59
	v_mfma_f32_32x32x16_f16 v[18:33], v[54:57], v[126:129], 0
	s_nop 6
	v_cvt_pk_f16_f32 v73, v72, v73
	v_cvt_pk_f16_f32 v72, v70, v71
	v_cvt_pk_f16_f32 v70, v66, v67
	v_cvt_pk_f16_f32 v67, v76, v77
	v_cvt_pk_f16_f32 v66, v74, v75
	global_load_dwordx4 v[74:77], v154, s[0:1]
	ds_read_b128 v[2:5], v181
	ds_read_b128 v[6:9], v177
	ds_read_b128 v[10:13], v181 offset:32768
	global_load_dwordx4 v[14:17], v154, s[0:1] offset:2048
	global_load_dwordx4 v[34:37], v154, s[0:1] offset:3072
	v_mfma_f32_32x32x16_f16 v[50:65], v[54:57], v[110:113], 0
	v_cvt_pk_f16_f32 v71, v68, v69
	v_cvt_pk_f16_f32 v69, v80, v81
	v_cvt_pk_f16_f32 v68, v78, v79
	v_mfma_f32_32x32x16_f16 v[18:33], v[82:85], v[122:125], v[18:33]
	v_mfma_f32_32x32x16_f16 v[50:65], v[82:85], v[106:109], v[50:65]
	ds_read_b128 v[82:85], v177 offset:32768
	v_mfma_f32_32x32x16_f16 v[18:33], v[70:73], v[118:121], v[18:33]
	v_mfma_f32_32x32x16_f16 v[50:65], v[70:73], v[94:97], v[50:65]
	v_mfma_f32_32x32x16_f16 v[18:33], v[66:69], v[114:117], v[18:33]
	v_mfma_f32_32x32x16_f16 v[50:65], v[66:69], v[90:93], v[50:65]
	s_nop 10
	v_cvt_pk_f16_f32 v25, v24, v25
	v_cvt_pk_f16_f32 v24, v22, v23
	v_cvt_pk_f16_f32 v23, v20, v21
	v_cvt_pk_f16_f32 v22, v18, v19
	ds_write_b128 v132, v[22:25]
	s_waitcnt vmcnt(2) lgkmcnt(4)
	v_mfma_f32_32x32x16_f16 v[66:81], v[2:5], v[74:77], 0
	s_waitcnt lgkmcnt(3)
	v_mfma_f32_32x32x16_f16 v[66:81], v[6:9], v[182:185], v[66:81]
	s_waitcnt vmcnt(1) lgkmcnt(2)
	v_mfma_f32_32x32x16_f16 v[66:81], v[10:13], v[14:17], v[66:81]
	s_waitcnt vmcnt(0) lgkmcnt(1)
	v_mfma_f32_32x32x16_f16 v[66:81], v[82:85], v[34:37], v[66:81]
	v_mfma_f32_32x32x16_f16 v[34:49], v[2:5], v[168:171], 0
	global_load_dwordx4 v[2:5], v[152:153], off offset:2048
	s_nop 9
	v_cvt_pk_f16_f32 v73, v72, v73
	v_cvt_pk_f16_f32 v72, v70, v71
	v_cvt_pk_f16_f32 v71, v68, v69
	v_cvt_pk_f16_f32 v70, v66, v67
	v_cvt_pk_f16_f32 v69, v80, v81
	v_cvt_pk_f16_f32 v68, v78, v79
	v_mfma_f32_32x32x16_f16 v[34:49], v[6:9], v[86:89], v[34:49]
	global_load_dwordx4 v[6:9], v[152:153], off offset:3072
	v_cvt_pk_f16_f32 v67, v76, v77
	v_cvt_pk_f16_f32 v66, v74, v75
	s_waitcnt vmcnt(1)
	v_mfma_f32_32x32x16_f16 v[34:49], v[10:13], v[2:5], v[34:49]
	s_waitcnt vmcnt(0)
	v_mfma_f32_32x32x16_f16 v[34:49], v[82:85], v[6:9], v[34:49]
	v_mfma_f32_32x32x16_f16 v[2:17], v[70:73], v[126:129], 0
	s_nop 10
	v_cvt_pk_f16_f32 v41, v40, v41
	v_cvt_pk_f16_f32 v40, v38, v39
	v_cvt_pk_f16_f32 v38, v34, v35
	v_cvt_pk_f16_f32 v35, v44, v45
	v_cvt_pk_f16_f32 v34, v42, v43
	v_cvt_pk_f16_f32 v45, v32, v33
	v_cvt_pk_f16_f32 v44, v30, v31
	v_cvt_pk_f16_f32 v43, v28, v29
	v_cvt_pk_f16_f32 v42, v26, v27
	v_mfma_f32_32x32x16_f16 v[18:33], v[70:73], v[110:113], 0
	v_cvt_pk_f16_f32 v39, v36, v37
	v_cvt_pk_f16_f32 v37, v48, v49
	v_cvt_pk_f16_f32 v36, v46, v47
	ds_write_b128 v131, v[42:45]
	v_cvt_pk_f16_f32 v45, v56, v57
	v_cvt_pk_f16_f32 v44, v54, v55
	v_cvt_pk_f16_f32 v43, v52, v53
	v_mfma_f32_32x32x16_f16 v[2:17], v[66:69], v[122:125], v[2:17]
	v_cvt_pk_f16_f32 v42, v50, v51
	ds_write_b128 v132, v[42:45] offset:32768
	v_cvt_pk_f16_f32 v45, v64, v65
	v_cvt_pk_f16_f32 v44, v62, v63
	v_cvt_pk_f16_f32 v43, v60, v61
	v_cvt_pk_f16_f32 v42, v58, v59
	ds_write_b128 v131, v[42:45] offset:32768
	v_mfma_f32_32x32x16_f16 v[18:33], v[66:69], v[106:109], v[18:33]
	v_mfma_f32_32x32x16_f16 v[2:17], v[38:41], v[118:121], v[2:17]
	v_mfma_f32_32x32x16_f16 v[18:33], v[38:41], v[94:97], v[18:33]
	v_mfma_f32_32x32x16_f16 v[2:17], v[34:37], v[114:117], v[2:17]
	v_mfma_f32_32x32x16_f16 v[18:33], v[34:37], v[90:93], v[18:33]
	s_nop 10
	v_cvt_pk_f16_f32 v9, v8, v9
	v_cvt_pk_f16_f32 v8, v6, v7
	v_cvt_pk_f16_f32 v7, v4, v5
	v_cvt_pk_f16_f32 v6, v2, v3
	v_cvt_pk_f16_f32 v5, v16, v17
	v_cvt_pk_f16_f32 v4, v14, v15
	v_cvt_pk_f16_f32 v3, v12, v13
	v_cvt_pk_f16_f32 v2, v10, v11
	ds_write_b128 v135, v[6:9]
	ds_write_b128 v133, v[2:5]
	v_cvt_pk_f16_f32 v5, v24, v25
	v_cvt_pk_f16_f32 v4, v22, v23
	v_cvt_pk_f16_f32 v3, v20, v21
	v_cvt_pk_f16_f32 v2, v18, v19
	ds_write_b128 v135, v[2:5] offset:32768
	v_cvt_pk_f16_f32 v5, v32, v33
	v_cvt_pk_f16_f32 v4, v30, v31
	v_cvt_pk_f16_f32 v3, v28, v29
	v_cvt_pk_f16_f32 v2, v26, v27
	ds_write_b128 v133, v[2:5] offset:32768
	s_setprio 0
	s_waitcnt lgkmcnt(0)
	s_barrier
	ds_read_b64_tr_b16 v[2:3], v146
	ds_read_b64_tr_b16 v[4:5], v147
	ds_read_b64_tr_b16 v[36:37], v147 offset:32768
	ds_read_b64_tr_b16 v[34:35], v146 offset:32768
	ds_read_b64_tr_b16 v[18:19], v150
	ds_read_b64_tr_b16 v[20:21], v151
	ds_read_b64_tr_b16 v[40:41], v151 offset:32768
	ds_read_b64_tr_b16 v[38:39], v150 offset:32768
	s_waitcnt lgkmcnt(6)
	v_mfma_f32_32x32x16_f16 v[2:17], v[2:5], v[102:105], 0
	ds_read_b64_tr_b16 v[42:43], v148
	ds_read_b64_tr_b16 v[44:45], v149
	ds_read_b64_tr_b16 v[48:49], v149 offset:32768
	ds_read_b64_tr_b16 v[46:47], v148 offset:32768
	v_cmp_gt_u32_e64 s[0:1], 32, v167
	s_cmp_eq_u32 s5, 0
	v_cmp_lt_i32_e64 s[2:3], v162, v163
	s_waitcnt lgkmcnt(6)
	v_mfma_f32_32x32x16_f16 v[18:33], v[18:21], v[102:105], 0
	v_mfma_f32_32x32x16_f16 v[2:17], v[34:37], v[98:101], v[2:17]
	s_waitcnt lgkmcnt(4)
	v_mfma_f32_32x32x16_f16 v[18:33], v[38:41], v[98:101], v[18:33]
	s_nop 9
	v_mul_f32_e64 v34, v16, v16
	v_mul_f32_e64 v35, v17, v17
	v_mul_f32_e64 v36, v12, v12
	v_mul_f32_e64 v37, v13, v13
	v_mul_f32_e64 v50, v8, v8
	v_mul_f32_e64 v51, v9, v9
	v_mul_f32_e32 v52, v4, v4
	v_mul_f32_e32 v53, v5, v5
	v_fma_f32 v50, v6, v6, v50
	v_fma_f32 v51, v7, v7, v51
	v_fma_f32 v52, v2, v2, v52
	v_fma_f32 v53, v3, v3, v53
	v_fma_f32 v36, v10, v10, v36
	v_fma_f32 v37, v11, v11, v37
	v_fma_f32 v34, v14, v14, v34
	v_fma_f32 v35, v15, v15, v35
	v_mul_f32_e32 v116, v24, v24
	v_mul_f32_e32 v117, v25, v25
	v_mul_f32_e32 v118, v20, v20
	v_mul_f32_e32 v119, v21, v21
	v_add_f32_e32 v50, v52, v50
	v_add_f32_e32 v51, v53, v51
	v_add_f32_e32 v34, v36, v34
	v_add_f32_e32 v35, v37, v35
	v_mul_f32_e32 v112, v32, v32
	v_mul_f32_e32 v113, v33, v33
	v_mul_f32_e32 v114, v28, v28
	v_mul_f32_e32 v115, v29, v29
	v_mul_f32_e32 v120, v18, v18
	v_mul_f32_e32 v121, v19, v19
	v_fma_f32 v18, v18, v18, v118
	v_fma_f32 v19, v19, v19, v119
	v_fma_f32 v20, v22, v22, v116
	v_fma_f32 v21, v23, v23, v117
	v_add_f32_e32 v34, v50, v34
	v_add_f32_e32 v35, v51, v35
	v_mul_f32_e32 v106, v22, v22
	v_mul_f32_e32 v107, v23, v23
	v_add_f32_e32 v18, v18, v20
	v_add_f32_e32 v19, v19, v21
	v_fma_f32 v20, v26, v26, v114
	v_fma_f32 v21, v27, v27, v115
	v_fma_f32 v22, v30, v30, v112
	v_fma_f32 v23, v31, v31, v113
	v_add_f32_e32 v34, v34, v35
	v_add_f32_e32 v20, v20, v22
	v_add_f32_e32 v21, v21, v23
	v_add_f32_e32 v36, 0, v34
	v_mul_f32_e32 v108, v26, v26
	v_mul_f32_e32 v109, v27, v27
	v_mul_f32_e32 v110, v30, v30
	v_mul_f32_e32 v111, v31, v31
	v_add_f32_e32 v34, v18, v20
	v_add_f32_e32 v35, v19, v21
	s_waitcnt lgkmcnt(2)
	v_mfma_f32_32x32x16_f16 v[18:33], v[42:45], v[102:105], 0
	v_add_f32_e32 v34, v34, v35
	v_add_f32_e32 v54, v36, v34
	v_sub_f32_e32 v55, v36, v34
	ds_read_b64_tr_b16 v[34:35], v144
	ds_read_b64_tr_b16 v[36:37], v145
	ds_read_b64_tr_b16 v[52:53], v145 offset:32768
	ds_read_b64_tr_b16 v[50:51], v144 offset:32768
	v_fma_f32 v4, v4, v4, v118
	v_fma_f32 v5, v5, v5, v119
	v_fma_f32 v16, v16, v16, v112
	v_fma_f32 v17, v17, v17, v113
	v_fma_f32 v14, v14, v14, v110
	v_fma_f32 v15, v15, v15, v111
	s_waitcnt lgkmcnt(4)
	v_mfma_f32_32x32x16_f16 v[18:33], v[46:49], v[98:101], v[18:33]
	v_fma_f32 v12, v12, v12, v114
	v_fma_f32 v13, v13, v13, v115
	v_fma_f32 v10, v10, v10, v108
	v_fma_f32 v11, v11, v11, v109
	v_fma_f32 v8, v8, v8, v116
	v_fma_f32 v9, v9, v9, v117
	v_fma_f32 v6, v6, v6, v106
	v_fma_f32 v7, v7, v7, v107
	v_fma_f32 v2, v2, v2, v120
	v_fma_f32 v3, v3, v3, v121
	s_nop 3
	v_mul_f32_e32 v38, v32, v32
	v_mul_f32_e32 v39, v33, v33
	v_mul_f32_e32 v40, v28, v28
	v_mul_f32_e32 v41, v29, v29
	v_mul_f32_e32 v42, v24, v24
	v_mul_f32_e32 v43, v25, v25
	v_mul_f32_e32 v44, v20, v20
	v_mul_f32_e32 v45, v21, v21
	v_fma_f32 v42, v22, v22, v42
	v_fma_f32 v43, v23, v23, v43
	v_fma_f32 v44, v18, v18, v44
	v_fma_f32 v45, v19, v19, v45
	v_fma_f32 v40, v26, v26, v40
	v_fma_f32 v41, v27, v27, v41
	v_fma_f32 v38, v30, v30, v38
	v_fma_f32 v39, v31, v31, v39
	v_add_f32_e32 v42, v44, v42
	v_add_f32_e32 v43, v45, v43
	v_add_f32_e32 v38, v40, v38
	v_add_f32_e32 v39, v41, v39
	v_fma_f32 v4, v20, v20, v4
	v_fma_f32 v5, v21, v21, v5
	v_add_f32_e32 v38, v42, v38
	v_add_f32_e32 v39, v43, v39
	v_fma_f32 v6, v22, v22, v6
	v_fma_f32 v7, v23, v23, v7
	v_add_f32_e32 v56, v38, v39
	s_waitcnt lgkmcnt(2)
	v_mfma_f32_32x32x16_f16 v[34:49], v[34:37], v[102:105], 0
	v_add_f32_e32 v70, v54, v56
	v_add_f32_e32 v71, v55, v56
	v_sub_f32_e32 v72, v54, v56
	ds_read_b64_tr_b16 v[54:55], v142
	ds_read_b64_tr_b16 v[56:57], v143
	ds_read_b64_tr_b16 v[68:69], v143 offset:32768
	ds_read_b64_tr_b16 v[66:67], v142 offset:32768
	v_fma_f32 v8, v24, v24, v8
	v_fma_f32 v9, v25, v25, v9
	v_fma_f32 v10, v26, v26, v10
	v_fma_f32 v11, v27, v27, v11
	v_fma_f32 v12, v28, v28, v12
	v_fma_f32 v13, v29, v29, v13
	s_waitcnt lgkmcnt(4)
	v_mfma_f32_32x32x16_f16 v[34:49], v[50:53], v[98:101], v[34:49]
	v_fma_f32 v14, v30, v30, v14
	v_fma_f32 v15, v31, v31, v15
	v_fma_f32 v16, v32, v32, v16
	v_fma_f32 v17, v33, v33, v17
	v_fma_f32 v2, v18, v18, v2
	v_fma_f32 v3, v19, v19, v3
	s_nop 5
	v_mul_f32_e32 v50, v48, v48
	v_mul_f32_e32 v51, v49, v49
	v_mul_f32_e32 v52, v44, v44
	v_mul_f32_e32 v53, v45, v45
	v_mul_f32_e32 v58, v40, v40
	v_mul_f32_e32 v59, v41, v41
	v_mul_f32_e32 v60, v36, v36
	v_mul_f32_e32 v61, v37, v37
	v_fma_f32 v58, v38, v38, v58
	v_fma_f32 v59, v39, v39, v59
	v_fma_f32 v60, v34, v34, v60
	v_fma_f32 v61, v35, v35, v61
	v_fma_f32 v52, v42, v42, v52
	v_fma_f32 v53, v43, v43, v53
	v_fma_f32 v50, v46, v46, v50
	v_fma_f32 v51, v47, v47, v51
	v_add_f32_e32 v58, v60, v58
	v_add_f32_e32 v59, v61, v59
	v_add_f32_e32 v50, v52, v50
	v_add_f32_e32 v51, v53, v51
	v_fma_f32 v4, v36, v36, v4
	v_fma_f32 v5, v37, v37, v5
	v_add_f32_e32 v50, v58, v50
	v_add_f32_e32 v51, v59, v51
	v_fma_f32 v16, v48, v48, v16
	v_fma_f32 v17, v49, v49, v17
	v_add_f32_e32 v73, v50, v51
	s_waitcnt lgkmcnt(2)
	v_mfma_f32_32x32x16_f16 v[50:65], v[54:57], v[102:105], 0
	v_add_f32_e32 v86, v70, v73
	v_sub_f32_e32 v87, v71, v73
	v_sub_f32_e32 v88, v72, v73
	ds_read_b64_tr_b16 v[70:71], v140
	ds_read_b64_tr_b16 v[72:73], v141
	ds_read_b64_tr_b16 v[84:85], v141 offset:32768
	ds_read_b64_tr_b16 v[82:83], v140 offset:32768
	v_fma_f32 v14, v46, v46, v14
	v_fma_f32 v15, v47, v47, v15
	v_fma_f32 v12, v44, v44, v12
	v_fma_f32 v13, v45, v45, v13
	v_fma_f32 v10, v42, v42, v10
	v_fma_f32 v11, v43, v43, v11
	s_waitcnt lgkmcnt(4)
	v_mfma_f32_32x32x16_f16 v[50:65], v[66:69], v[98:101], v[50:65]
	v_fma_f32 v8, v40, v40, v8
	v_fma_f32 v9, v41, v41, v9
	v_fma_f32 v6, v38, v38, v6
	v_fma_f32 v7, v39, v39, v7
	v_fma_f32 v2, v34, v34, v2
	v_fma_f32 v3, v35, v35, v3
	s_nop 5
	v_mul_f32_e32 v66, v64, v64
	v_mul_f32_e32 v67, v65, v65
	v_mul_f32_e32 v68, v60, v60
	v_mul_f32_e32 v69, v61, v61
	v_mul_f32_e32 v74, v56, v56
	v_mul_f32_e32 v75, v57, v57
	v_mul_f32_e32 v76, v52, v52
	v_mul_f32_e32 v77, v53, v53
	v_fma_f32 v74, v54, v54, v74
	v_fma_f32 v75, v55, v55, v75
	v_fma_f32 v76, v50, v50, v76
	v_fma_f32 v77, v51, v51, v77
	v_fma_f32 v68, v58, v58, v68
	v_fma_f32 v69, v59, v59, v69
	v_fma_f32 v66, v62, v62, v66
	v_fma_f32 v67, v63, v63, v67
	v_add_f32_e32 v74, v76, v74
	v_add_f32_e32 v75, v77, v75
	v_add_f32_e32 v66, v68, v66
	v_add_f32_e32 v67, v69, v67
	v_fma_f32 v4, v52, v52, v4
	v_fma_f32 v5, v53, v53, v5
	v_add_f32_e32 v66, v74, v66
	v_add_f32_e32 v67, v75, v67
	v_fma_f32 v6, v54, v54, v6
	v_fma_f32 v7, v55, v55, v7
	v_add_f32_e32 v89, v66, v67
	s_waitcnt lgkmcnt(2)
	v_mfma_f32_32x32x16_f16 v[66:81], v[70:73], v[102:105], 0
	v_add_f32_e32 v94, v86, v89
	v_add_f32_e32 v126, v87, v89
	v_add_f32_e32 v127, v88, v89
	v_sub_f32_e32 v128, v86, v89
	ds_read_b64_tr_b16 v[86:87], v138
	ds_read_b64_tr_b16 v[88:89], v139
	ds_read_b64_tr_b16 v[124:125], v139 offset:32768
	ds_read_b64_tr_b16 v[122:123], v138 offset:32768
	v_fma_f32 v8, v56, v56, v8
	v_fma_f32 v9, v57, v57, v9
	v_fma_f32 v10, v58, v58, v10
	v_fma_f32 v11, v59, v59, v11
	s_waitcnt lgkmcnt(4)
	v_mfma_f32_32x32x16_f16 v[66:81], v[82:85], v[98:101], v[66:81]
	v_fma_f32 v12, v60, v60, v12
	v_fma_f32 v13, v61, v61, v13
	v_fma_f32 v14, v62, v62, v14
	v_fma_f32 v15, v63, v63, v15
	v_fma_f32 v16, v64, v64, v16
	v_fma_f32 v17, v65, v65, v17
	v_fma_f32 v2, v50, v50, v2
	v_fma_f32 v3, v51, v51, v3
	s_nop 4
	v_mul_f32_e32 v82, v80, v80
	v_mul_f32_e32 v83, v81, v81
	v_mul_f32_e32 v84, v76, v76
	v_mul_f32_e32 v85, v77, v77
	v_mul_f32_e32 v90, v72, v72
	v_mul_f32_e32 v91, v73, v73
	v_mul_f32_e32 v92, v68, v68
	v_mul_f32_e32 v93, v69, v69
	v_fma_f32 v90, v70, v70, v90
	v_fma_f32 v91, v71, v71, v91
	v_fma_f32 v92, v66, v66, v92
	v_fma_f32 v93, v67, v67, v93
	v_fma_f32 v84, v74, v74, v84
	v_fma_f32 v85, v75, v75, v85
	v_fma_f32 v82, v78, v78, v82
	v_fma_f32 v83, v79, v79, v83
	v_add_f32_e32 v90, v92, v90
	v_add_f32_e32 v91, v93, v91
	v_add_f32_e32 v82, v84, v82
	v_add_f32_e32 v83, v85, v83
	v_fma_f32 v4, v68, v68, v4
	v_fma_f32 v5, v69, v69, v5
	v_add_f32_e32 v82, v90, v82
	v_add_f32_e32 v83, v91, v83
	v_fma_f32 v18, v80, v80, v16
	v_fma_f32 v19, v81, v81, v17
	v_add_f32_e32 v129, v82, v83
	v_add_f32_e32 v131, v94, v129
	s_waitcnt lgkmcnt(2)
	v_mfma_f32_32x32x16_f16 v[82:97], v[86:89], v[102:105], 0
	v_sub_f32_e32 v135, v126, v129
	v_add_f32_e32 v142, v127, v129
	v_sub_f32_e32 v143, v128, v129
	ds_read_b64_tr_b16 v[126:127], v136
	ds_read_b64_tr_b16 v[128:129], v137
	ds_read_b64_tr_b16 v[138:139], v137 offset:32768
	ds_read_b64_tr_b16 v[136:137], v136 offset:32768
	v_fma_f32 v20, v78, v78, v14
	v_fma_f32 v21, v79, v79, v15
	v_fma_f32 v22, v76, v76, v12
	v_fma_f32 v23, v77, v77, v13
	v_fma_f32 v24, v74, v74, v10
	v_fma_f32 v25, v75, v75, v11
	s_waitcnt lgkmcnt(4)
	v_mfma_f32_32x32x16_f16 v[82:97], v[122:125], v[98:101], v[82:97]
	v_fma_f32 v26, v72, v72, v8
	v_fma_f32 v27, v73, v73, v9
	v_fma_f32 v28, v70, v70, v6
	v_fma_f32 v29, v71, v71, v7
	v_fma_f32 v30, v66, v66, v2
	v_fma_f32 v31, v67, v67, v3
	s_nop 5
	v_fma_f32 v32, v84, v84, v4
	v_fma_f32 v33, v85, v85, v5
	s_waitcnt lgkmcnt(2)
	v_mfma_f32_32x32x16_f16 v[2:17], v[126:129], v[102:105], 0
	v_fma_f32 v28, v86, v86, v28
	v_fma_f32 v29, v87, v87, v29
	v_fma_f32 v24, v90, v90, v24
	v_fma_f32 v25, v91, v91, v25
	v_fma_f32 v22, v92, v92, v22
	v_fma_f32 v23, v93, v93, v23
	v_fma_f32 v20, v94, v94, v20
	v_fma_f32 v21, v95, v95, v21
	v_fma_f32 v18, v96, v96, v18
	v_fma_f32 v19, v97, v97, v19
	v_fma_f32 v30, v82, v82, v30
	v_fma_f32 v31, v83, v83, v31
	v_fma_f32 v26, v88, v88, v26
	v_fma_f32 v27, v89, v89, v27
	s_waitcnt lgkmcnt(0)
	v_mfma_f32_32x32x16_f16 v[2:17], v[136:139], v[98:101], v[2:17]
	v_mul_f32_e64 v122, v96, v96
	v_mul_f32_e64 v123, v97, v97
	v_mul_f32_e64 v124, v92, v92
	v_mul_f32_e64 v125, v93, v93
	v_mul_f32_e64 v132, v88, v88
	v_mul_f32_e64 v133, v89, v89
	v_mul_f32_e32 v140, v84, v84
	v_mul_f32_e32 v141, v85, v85
	v_fma_f32 v132, v86, v86, v132
	v_fma_f32 v133, v87, v87, v133
	v_fma_f32 v140, v82, v82, v140
	v_fma_f32 v141, v83, v83, v141
	v_fma_f32 v124, v90, v90, v124
	v_fma_f32 v125, v91, v91, v125
	s_nop 1
	v_mul_f32_e32 v38, v8, v8
	v_mul_f32_e32 v39, v9, v9
	v_mul_f32_e32 v40, v4, v4
	v_mul_f32_e32 v41, v5, v5
	v_mul_f32_e32 v34, v16, v16
	v_mul_f32_e32 v35, v17, v17
	v_mul_f32_e32 v36, v12, v12
	v_mul_f32_e32 v37, v13, v13
	v_fma_f32 v16, v16, v16, v18
	v_fma_f32 v17, v17, v17, v19
	v_fma_f32 v18, v14, v14, v20
	v_fma_f32 v19, v15, v15, v21
	v_fma_f32 v12, v12, v12, v22
	v_fma_f32 v13, v13, v13, v23
	v_fma_f32 v20, v10, v10, v24
	v_fma_f32 v21, v11, v11, v25
	v_fma_f32 v22, v6, v6, v28
	v_fma_f32 v23, v7, v7, v29
	v_fma_f32 v24, v2, v2, v30
	v_fma_f32 v25, v3, v3, v31
	v_fma_f32 v2, v2, v2, v40
	v_fma_f32 v3, v3, v3, v41
	v_fma_f32 v6, v6, v6, v38
	v_fma_f32 v7, v7, v7, v39
	v_fma_f32 v4, v4, v4, v32
	v_fma_f32 v5, v5, v5, v33
	v_add_f32_e32 v2, v2, v6
	v_add_f32_e32 v3, v3, v7
	v_fma_f32 v6, v10, v10, v36
	v_fma_f32 v7, v11, v11, v37
	v_fma_f32 v10, v14, v14, v34
	v_fma_f32 v11, v15, v15, v35
	v_fma_f32 v8, v8, v8, v26
	v_fma_f32 v9, v9, v9, v27
	v_add_f32_e32 v6, v6, v10
	v_add_f32_e32 v7, v7, v11
	v_sub_f32_e32 v10, v24, v25
	v_add_f32_e32 v11, v25, v24
	v_add_f32_e32 v10, v4, v10
	v_sub_f32_e32 v14, v11, v4
	v_add_f32_e32 v4, v4, v11
	v_sub_f32_e32 v10, v10, v5
	v_sub_f32_e32 v11, v14, v5
	v_add_f32_e32 v4, v5, v4
	v_add_f32_e32 v5, v22, v10
	v_add_f32_e32 v10, v22, v11
	v_sub_f32_e32 v11, v4, v22
	v_add_f32_e32 v4, v22, v4
	v_sub_f32_e32 v5, v5, v23
	v_add_f32_e32 v10, v23, v10
	v_sub_f32_e32 v11, v11, v23
	v_add_f32_e32 v4, v23, v4
	v_add_f32_e32 v5, v8, v5
	v_sub_f32_e32 v10, v10, v8
	v_sub_f32_e32 v11, v11, v8
	v_add_f32_e32 v4, v8, v4
	v_sub_f32_e32 v5, v5, v9
	v_fma_f32 v122, v94, v94, v122
	v_fma_f32 v123, v95, v95, v123
	v_sub_f32_e32 v8, v10, v9
	v_sub_f32_e32 v10, v11, v9
	v_add_f32_e32 v4, v9, v4
	v_add_f32_e32 v5, v20, v5
	v_add_f32_e32 v132, v140, v132
	v_add_f32_e32 v133, v141, v133
	v_add_f32_e32 v122, v124, v122
	v_add_f32_e32 v123, v125, v123
	v_add_f32_e32 v8, v20, v8
	v_add_f32_e32 v9, v20, v10
	v_sub_f32_e32 v4, v4, v20
	v_sub_f32_e32 v5, v5, v21
	v_add_f32_e32 v122, v132, v122
	v_add_f32_e32 v123, v133, v123
	v_add_f32_e32 v8, v21, v8
	v_add_f32_e32 v9, v21, v9
	v_sub_f32_e32 v4, v4, v21
	v_add_f32_e32 v5, v12, v5
	v_add_f32_e32 v122, v122, v123
	v_add_f32_e32 v2, v2, v6
	v_add_f32_e32 v3, v3, v7
	v_sub_f32_e32 v8, v8, v12
	v_add_f32_e32 v9, v12, v9
	v_sub_f32_e32 v4, v4, v12
	v_sub_f32_e32 v5, v5, v13
	v_add_f32_e32 v123, v131, v122
	v_add_f32_e32 v2, v2, v3
	v_sub_f32_e32 v8, v8, v13
	v_add_f32_e32 v9, v13, v9
	v_sub_f32_e32 v4, v4, v13
	v_add_f32_e32 v5, v18, v5
	v_add_f32_e32 v3, v123, v2
	v_add_f32_e32 v8, v18, v8
	v_sub_f32_e32 v9, v9, v18
	v_sub_f32_e32 v4, v4, v18
	v_sub_f32_e32 v5, v5, v19
	v_and_b32_e32 v10, 8, v156
	v_add_f32_e32 v8, v19, v8
	v_sub_f32_e32 v9, v9, v19
	v_sub_f32_e32 v4, v4, v19
	v_add_f32_e32 v5, v16, v5
	v_cmp_eq_u32_e32 vcc, 0, v10
	v_cndmask_b32_e64 v10, -v3, v3, s[0:1]
	s_cselect_b64 s[0:1], -1, 0
	s_bitcmp0_b32 s4, 7
	v_sub_f32_e32 v8, v8, v16
	v_sub_f32_e32 v9, v9, v16
	v_sub_f32_e32 v4, v4, v16
	v_sub_f32_e32 v5, v5, v17
	v_cndmask_b32_e64 v11, -v3, v3, s[0:1]
	s_cselect_b64 s[0:1], -1, 0
	v_and_b32_e32 v16, 32, v156
	v_sub_f32_e32 v8, v8, v17
	v_cndmask_b32_e64 v5, -v5, v5, vcc
	v_cndmask_b32_e64 v12, -v3, v3, s[0:1]
	v_cndmask_b32_e64 v18, v161, v162, s[2:3]
	v_cmp_eq_u32_e64 s[2:3], 0, v16
	v_lshlrev_b32_e32 v18, 2, v18
	v_cmp_eq_u32_e64 s[0:1], 0, v134
	v_cndmask_b32_e64 v16, v11, v5, s[2:3]
	v_cndmask_b32_e64 v5, v5, v11, s[2:3]
	v_cndmask_b32_e64 v11, v8, v12, s[2:3]
	ds_bpermute_b32 v11, v18, v11
	v_and_b32_e32 v14, 2, v156
	v_cndmask_b32_e64 v13, -v3, v3, s[0:1]
	v_cmp_eq_u32_e64 s[0:1], 0, v14
	v_cndmask_b32_e64 v8, v12, v8, s[2:3]
	v_add_f32_e32 v124, v135, v122
	v_cndmask_b32_e64 v14, -v3, v3, s[0:1]
	v_cmp_eq_u32_e64 s[0:1], 0, v130
	v_sub_f32_e32 v4, v4, v17
	s_waitcnt lgkmcnt(0)
	v_add_f32_e32 v8, v8, v11
	v_cndmask_b32_e64 v15, -v3, v3, s[0:1]
	v_cndmask_b32_e64 v11, v14, v10, s[2:3]
	v_cndmask_b32_e64 v10, v10, v14, s[2:3]
	v_sub_f32_e32 v6, v124, v2
	v_sub_f32_e32 v9, v9, v17
	v_cndmask_b32_e64 v3, -v3, v3, vcc
	ds_bpermute_b32 v10, v18, v10
	v_cndmask_b32_e64 v12, v4, v15, s[2:3]
	v_sub_f32_e32 v125, v142, v122
	v_cndmask_b32_e64 v19, v9, v13, s[2:3]
	v_cndmask_b32_e64 v9, v13, v9, s[2:3]
	ds_bpermute_b32 v12, v18, v12
	v_cndmask_b32_e64 v13, v6, v3, s[2:3]
	v_sub_f32_e32 v7, v125, v2
	v_bfe_i32 v17, v156, 5, 1
	ds_bpermute_b32 v5, v18, v5
	ds_bpermute_b32 v13, v18, v13
	v_sub_f32_e32 v122, v143, v122
	v_cndmask_b32_e64 v3, v3, v6, s[2:3]
	v_and_b32_e32 v6, v17, v7
	v_sub_f32_e32 v2, v122, v2
	ds_bpermute_b32 v19, v18, v19
	ds_bpermute_b32 v6, v18, v6
	s_waitcnt lgkmcnt(5)
	v_add_f32_e32 v10, v11, v10
	v_cndmask_b32_e64 v4, v15, v4, s[2:3]
	v_and_b32_e32 v11, v17, v2
	s_waitcnt lgkmcnt(4)
	v_add_f32_e32 v4, v4, v12
	ds_bpermute_b32 v11, v18, v11
	v_and_b32_e32 v12, 16, v156
	v_cmp_lt_i32_e64 s[4:5], v164, v163
	s_waitcnt lgkmcnt(4)
	v_add_f32_e32 v5, v16, v5
	s_waitcnt lgkmcnt(3)
	v_add_f32_e32 v3, v3, v13
	v_cndmask_b32_e64 v13, v161, v164, s[4:5]
	v_cmp_eq_u32_e64 s[4:5], 0, v12
	s_waitcnt lgkmcnt(2)
	v_add_f32_e32 v9, v9, v19
	v_lshlrev_b32_e32 v13, 2, v13
	v_cndmask_b32_e64 v12, v4, v5, s[4:5]
	v_cndmask_b32_e64 v4, v5, v4, s[4:5]
	v_cndmask_b32_e64 v5, 0, v7, s[2:3]
	s_waitcnt lgkmcnt(1)
	v_add_f32_e32 v5, v5, v6
	v_cndmask_b32_e64 v2, 0, v2, s[2:3]
	v_cndmask_b32_e64 v7, v9, v5, s[4:5]
	ds_bpermute_b32 v4, v13, v4
	s_waitcnt lgkmcnt(1)
	v_add_f32_e32 v2, v2, v11
	v_cndmask_b32_e64 v6, v3, v8, s[4:5]
	v_cndmask_b32_e64 v3, v8, v3, s[4:5]
	ds_bpermute_b32 v7, v13, v7
	ds_bpermute_b32 v3, v13, v3
	v_cndmask_b32_e64 v8, v10, v2, s[4:5]
	ds_bpermute_b32 v8, v13, v8
	v_cndmask_b32_e64 v5, v5, v9, s[4:5]
	s_waitcnt lgkmcnt(3)
	v_add_f32_e32 v4, v12, v4
	s_waitcnt lgkmcnt(2)
	v_add_f32_e32 v5, v5, v7
	s_waitcnt lgkmcnt(1)
	v_add_f32_e32 v3, v6, v3
	v_cndmask_b32_e64 v2, v2, v10, s[4:5]
	v_cndmask_b32_e32 v6, v5, v4, vcc
	v_cndmask_b32_e32 v4, v4, v5, vcc
	v_mov_b32_e32 v5, v155
	s_waitcnt lgkmcnt(0)
	v_add_f32_e32 v2, v2, v8
	v_mov_b32_dpp v5, v4 row_mirror row_mask:0xf bank_mask:0xf
	s_nop 1
	v_add_f32_dpp v4, v5, v6 row_half_mirror row_mask:0xf bank_mask:0xf bound_ctrl:1
	v_cndmask_b32_e32 v5, v2, v3, vcc
	v_cndmask_b32_e32 v2, v3, v2, vcc
	v_mov_b32_e32 v3, v155
	s_nop 1
	v_mov_b32_dpp v3, v2 row_mirror row_mask:0xf bank_mask:0xf
	s_nop 1
	v_add_f32_dpp v2, v3, v5 row_half_mirror row_mask:0xf bank_mask:0xf bound_ctrl:1
	v_cndmask_b32_e64 v3, v2, v4, s[0:1]
	v_cndmask_b32_e64 v2, v4, v2, s[0:1]
	v_mov_b32_e32 v4, v155
	s_nop 1
	v_mov_b32_dpp v4, v2 row_half_mirror row_mask:0xf bank_mask:0xf
	s_nop 1
	v_add_f32_dpp v2, v4, v3 quad_perm:[3,2,1,0] row_mask:0xf bank_mask:0xf bound_ctrl:1
	v_and_b32_e32 v4, 3, v156
	v_cmp_eq_u32_e32 vcc, 0, v4
	v_and_b32_e32 v4, 56, v156
	v_add_f32_dpp v2, v2, v2 quad_perm:[2,3,0,1] row_mask:0xf bank_mask:0xf bound_ctrl:1
	v_mov_b32_e32 v3, 0
	v_cmp_ne_u32_e64 s[0:1], 56, v4
	s_and_b64 s[2:3], vcc, s[0:1]
	v_mov_b32_dpp v3, v2 quad_perm:[1,0,3,2] row_mask:0xf bank_mask:0xf
	s_and_saveexec_b64 s[0:1], s[2:3]
	v_and_b32_e32 v4, 0xfc, v156
	v_add_f32_e32 v2, v2, v3
	v_or_b32_e32 v4, v165, v4
	ds_write_b32 v4, v2
	s_or_b64 exec, exec, s[0:1]
	v_cmp_gt_i32_e32 vcc, 14, v156
	s_waitcnt lgkmcnt(0)
	s_barrier
	s_and_saveexec_b64 s[0:1], vcc
	s_cbranch_execz .LBB1_2
	ds_read_b32 v2, v166
	ds_read_b32 v3, v166 offset:64
	ds_read_b32 v4, v166 offset:128
	ds_read_b32 v5, v166 offset:192
	s_waitcnt lgkmcnt(2)
	v_add_f32_e32 v2, v2, v3
	s_waitcnt lgkmcnt(1)
	v_add_f32_e32 v2, v2, v4
	s_waitcnt lgkmcnt(0)
	v_add_f32_e32 v2, v2, v5
	v_mul_f32_e32 v4, 0x39800000, v2
	v_lshl_add_u64 v[2:3], v[156:157], 2, s[14:15]
	global_store_dword v[2:3], v4, off
	s_branch .LBB1_2
